# speedup vs baseline: 1.0042x; 1.0042x over previous
.LBB6_12:
	ds_read_b128 v[176:179], v169
	ds_read_b128 v[180:183], v170
	ds_read_b128 v[184:187], v171
	ds_read_b128 v[188:191], v172
	v_add_u32_e32 v174, 0xc000, v152
	v_lshl_add_u64 v[192:193], v[136:137], 0, s[44:45]
	v_add_u32_e32 v175, 0xe000, v152
	v_add_u32_e32 v173, s17, v168
	v_lshl_add_u64 v[232:233], v[192:193], 0, s[30:31]
	s_mov_b32 m0, s72
	v_lshl_add_u64 v[248:249], v[134:135], 0, s[44:45]
	ds_read_b128 v[196:199], v173
	ds_read_b128 v[200:203], v173 offset:1024
	ds_read_b128 v[204:207], v173 offset:2048
	ds_read_b128 v[212:215], v173 offset:3072
	ds_read_b128 v[216:219], v173 offset:4096
	ds_read_b128 v[220:223], v173 offset:5120
	ds_read_b128 v[224:227], v173 offset:6144
	ds_read_b128 v[228:231], v173 offset:7168
	global_load_lds_dwordx4 v[232:233], off
	s_mov_b32 m0, s73
	v_lshl_add_u64 v[232:233], v[248:249], 0, s[30:31]
	global_load_lds_dwordx4 v[232:233], off
	s_waitcnt lgkmcnt(8)
	s_barrier
	s_waitcnt lgkmcnt(0)
	v_mfma_f32_16x16x32_f16 v[2:5], v[196:199], v[176:179], v[2:5]
	v_mfma_f32_16x16x32_f16 v[6:9], v[196:199], v[184:187], v[6:9]
	v_mfma_f32_16x16x32_f16 v[10:13], v[204:207], v[176:179], v[10:13]
	v_mfma_f32_16x16x32_f16 v[18:21], v[204:207], v[184:187], v[18:21]
	v_mfma_f32_16x16x32_f16 v[30:33], v[216:219], v[176:179], v[30:33]
	v_mfma_f32_16x16x32_f16 v[42:45], v[216:219], v[184:187], v[42:45]
	v_mfma_f32_16x16x32_f16 v[54:57], v[224:227], v[176:179], v[54:57]
	v_mfma_f32_16x16x32_f16 v[66:69], v[224:227], v[184:187], v[66:69]
	v_mfma_f32_16x16x32_f16 v[2:5], v[200:203], v[180:183], v[2:5]
	v_mfma_f32_16x16x32_f16 v[6:9], v[200:203], v[188:191], v[6:9]
	v_mfma_f32_16x16x32_f16 v[10:13], v[212:215], v[180:183], v[10:13]
	v_mfma_f32_16x16x32_f16 v[18:21], v[212:215], v[188:191], v[18:21]
	v_mfma_f32_16x16x32_f16 v[30:33], v[220:223], v[180:183], v[30:33]
	v_mfma_f32_16x16x32_f16 v[42:45], v[220:223], v[188:191], v[42:45]
	v_mfma_f32_16x16x32_f16 v[54:57], v[228:231], v[180:183], v[54:57]
	v_mfma_f32_16x16x32_f16 v[66:69], v[228:231], v[188:191], v[66:69]
	s_barrier
	v_lshl_add_u64 v[250:251], v[140:141], 0, s[44:45]
	s_mov_b32 m0, s74
	v_lshl_add_u64 v[252:253], v[250:251], 0, s[34:35]
	global_load_lds_dwordx4 v[252:253], off
	ds_read_b128 v[232:235], v161
	ds_read_b128 v[236:239], v162
	ds_read_b128 v[240:243], v163
	ds_read_b128 v[244:247], v164
	v_lshl_add_u64 v[252:253], v[138:139], 0, s[44:45]
	s_mov_b32 m0, s75
	v_lshl_add_u64 v[254:255], v[252:253], 0, s[34:35]
	global_load_lds_dwordx4 v[254:255], off
	s_barrier
	s_waitcnt lgkmcnt(0)
	v_mfma_f32_16x16x32_f16 v[14:17], v[196:199], v[232:235], v[14:17]
	v_mfma_f32_16x16x32_f16 v[22:25], v[196:199], v[240:243], v[22:25]
	v_mfma_f32_16x16x32_f16 v[34:37], v[204:207], v[232:235], v[34:37]
	v_mfma_f32_16x16x32_f16 v[46:49], v[204:207], v[240:243], v[46:49]
	v_mfma_f32_16x16x32_f16 v[58:61], v[216:219], v[232:235], v[58:61]
	v_mfma_f32_16x16x32_f16 v[70:73], v[216:219], v[240:243], v[70:73]
	v_mfma_f32_16x16x32_f16 v[78:81], v[224:227], v[232:235], v[78:81]
	v_mfma_f32_16x16x32_f16 v[86:89], v[224:227], v[240:243], v[86:89]
	v_mfma_f32_16x16x32_f16 v[14:17], v[200:203], v[236:239], v[14:17]
	v_mfma_f32_16x16x32_f16 v[22:25], v[200:203], v[244:247], v[22:25]
	v_mfma_f32_16x16x32_f16 v[34:37], v[212:215], v[236:239], v[34:37]
	v_mfma_f32_16x16x32_f16 v[46:49], v[212:215], v[244:247], v[46:49]
	v_mfma_f32_16x16x32_f16 v[58:61], v[220:223], v[236:239], v[58:61]
	v_mfma_f32_16x16x32_f16 v[70:73], v[220:223], v[244:247], v[70:73]
	v_mfma_f32_16x16x32_f16 v[78:81], v[228:231], v[236:239], v[78:81]
	v_mfma_f32_16x16x32_f16 v[86:89], v[228:231], v[244:247], v[86:89]
	v_lshl_add_u64 v[254:255], v[192:193], 0, s[34:35]
	s_mov_b32 m0, s76
	s_barrier
	ds_read_b128 v[196:199], v173 offset:16384
	ds_read_b128 v[200:203], v173 offset:17408
	ds_read_b128 v[204:207], v173 offset:18432
	ds_read_b128 v[212:215], v173 offset:19456
	ds_read_b128 v[216:219], v173 offset:20480
	ds_read_b128 v[220:223], v173 offset:21504
	ds_read_b128 v[224:227], v173 offset:22528
	ds_read_b128 v[228:231], v173 offset:23552
	global_load_lds_dwordx4 v[254:255], off
	s_mov_b32 m0, s77
	v_lshl_add_u64 v[254:255], v[248:249], 0, s[34:35]
	global_load_lds_dwordx4 v[254:255], off
	s_barrier
	s_waitcnt lgkmcnt(0)
	v_mfma_f32_16x16x32_f16 v[26:29], v[196:199], v[176:179], v[26:29]
	v_mfma_f32_16x16x32_f16 v[38:41], v[196:199], v[184:187], v[38:41]
	v_mfma_f32_16x16x32_f16 v[50:53], v[204:207], v[176:179], v[50:53]
	v_mfma_f32_16x16x32_f16 v[62:65], v[204:207], v[184:187], v[62:65]
	v_mfma_f32_16x16x32_f16 v[74:77], v[216:219], v[176:179], v[74:77]
	v_mfma_f32_16x16x32_f16 v[82:85], v[216:219], v[184:187], v[82:85]
	v_mfma_f32_16x16x32_f16 v[90:93], v[224:227], v[176:179], v[90:93]
	v_mfma_f32_16x16x32_f16 v[94:97], v[224:227], v[184:187], v[94:97]
	v_mfma_f32_16x16x32_f16 v[26:29], v[200:203], v[180:183], v[26:29]
	v_mfma_f32_16x16x32_f16 v[38:41], v[200:203], v[188:191], v[38:41]
	v_mfma_f32_16x16x32_f16 v[50:53], v[212:215], v[180:183], v[50:53]
	v_mfma_f32_16x16x32_f16 v[62:65], v[212:215], v[188:191], v[62:65]
	v_mfma_f32_16x16x32_f16 v[74:77], v[220:223], v[180:183], v[74:77]
	v_mfma_f32_16x16x32_f16 v[82:85], v[220:223], v[188:191], v[82:85]
	v_mfma_f32_16x16x32_f16 v[90:93], v[228:231], v[180:183], v[90:93]
	v_mfma_f32_16x16x32_f16 v[94:97], v[228:231], v[188:191], v[94:97]
	s_barrier
	s_mov_b32 m0, s78
	v_lshl_add_u64 v[176:177], v[250:251], 0, s[36:37]
	global_load_lds_dwordx4 v[176:177], off
	s_mov_b32 m0, s79
	v_lshl_add_u64 v[176:177], v[252:253], 0, s[36:37]
	global_load_lds_dwordx4 v[176:177], off
	s_waitcnt vmcnt(6)
	s_barrier
	v_mfma_f32_16x16x32_f16 v[98:101], v[196:199], v[232:235], v[98:101]
	v_mfma_f32_16x16x32_f16 v[102:105], v[196:199], v[240:243], v[102:105]
	v_mfma_f32_16x16x32_f16 v[106:109], v[204:207], v[232:235], v[106:109]
	v_mfma_f32_16x16x32_f16 v[110:113], v[204:207], v[240:243], v[110:113]
	v_mfma_f32_16x16x32_f16 v[114:117], v[216:219], v[232:235], v[114:117]
	v_mfma_f32_16x16x32_f16 v[118:121], v[216:219], v[240:243], v[118:121]
	v_mfma_f32_16x16x32_f16 v[122:125], v[224:227], v[232:235], v[122:125]
	v_mfma_f32_16x16x32_f16 v[126:129], v[224:227], v[240:243], v[126:129]
	v_mfma_f32_16x16x32_f16 v[98:101], v[200:203], v[236:239], v[98:101]
	v_mfma_f32_16x16x32_f16 v[102:105], v[200:203], v[244:247], v[102:105]
	v_mfma_f32_16x16x32_f16 v[106:109], v[212:215], v[236:239], v[106:109]
	v_mfma_f32_16x16x32_f16 v[110:113], v[212:215], v[244:247], v[110:113]
	v_mfma_f32_16x16x32_f16 v[114:117], v[220:223], v[236:239], v[114:117]
	v_mfma_f32_16x16x32_f16 v[118:121], v[220:223], v[244:247], v[118:121]
	v_mfma_f32_16x16x32_f16 v[122:125], v[228:231], v[236:239], v[122:125]
	v_mfma_f32_16x16x32_f16 v[126:129], v[228:231], v[244:247], v[126:129]
	s_barrier
	ds_read_b128 v[176:179], v148
	ds_read_b128 v[180:183], v149
	ds_read_b128 v[184:187], v150
	ds_read_b128 v[188:191], v151
	s_mov_b32 m0, s80
	v_lshl_add_u64 v[232:233], v[192:193], 0, s[36:37]
	global_load_lds_dwordx4 v[232:233], off
	ds_read_b128 v[196:199], v173 offset:32768
	ds_read_b128 v[200:203], v173 offset:33792
	ds_read_b128 v[204:207], v173 offset:34816
	ds_read_b128 v[212:215], v173 offset:35840
	ds_read_b128 v[216:219], v173 offset:36864
	ds_read_b128 v[220:223], v173 offset:37888
	ds_read_b128 v[224:227], v173 offset:38912
	ds_read_b128 v[228:231], v173 offset:39936
	s_mov_b32 m0, s81
	v_lshl_add_u64 v[232:233], v[248:249], 0, s[36:37]
	global_load_lds_dwordx4 v[232:233], off
	s_waitcnt lgkmcnt(8)
	s_barrier
	s_waitcnt lgkmcnt(0)
	v_mfma_f32_16x16x32_f16 v[2:5], v[196:199], v[176:179], v[2:5]
	v_mfma_f32_16x16x32_f16 v[6:9], v[196:199], v[184:187], v[6:9]
	v_mfma_f32_16x16x32_f16 v[10:13], v[204:207], v[176:179], v[10:13]
	v_mfma_f32_16x16x32_f16 v[18:21], v[204:207], v[184:187], v[18:21]
	v_mfma_f32_16x16x32_f16 v[30:33], v[216:219], v[176:179], v[30:33]
	v_mfma_f32_16x16x32_f16 v[42:45], v[216:219], v[184:187], v[42:45]
	v_mfma_f32_16x16x32_f16 v[54:57], v[224:227], v[176:179], v[54:57]
	v_mfma_f32_16x16x32_f16 v[66:69], v[224:227], v[184:187], v[66:69]
	v_mfma_f32_16x16x32_f16 v[2:5], v[200:203], v[180:183], v[2:5]
	v_mfma_f32_16x16x32_f16 v[6:9], v[200:203], v[188:191], v[6:9]
	v_mfma_f32_16x16x32_f16 v[10:13], v[212:215], v[180:183], v[10:13]
	v_mfma_f32_16x16x32_f16 v[18:21], v[212:215], v[188:191], v[18:21]
	v_mfma_f32_16x16x32_f16 v[30:33], v[220:223], v[180:183], v[30:33]
	v_mfma_f32_16x16x32_f16 v[42:45], v[220:223], v[188:191], v[42:45]
	v_mfma_f32_16x16x32_f16 v[54:57], v[228:231], v[180:183], v[54:57]
	v_mfma_f32_16x16x32_f16 v[66:69], v[228:231], v[188:191], v[66:69]
	s_barrier
	s_mov_b32 m0, s82
	v_lshl_add_u64 v[254:255], v[250:251], 0, s[38:39]
	global_load_lds_dwordx4 v[254:255], off
	ds_read_b128 v[232:235], v142
	ds_read_b128 v[236:239], v143
	ds_read_b128 v[240:243], v144
	ds_read_b128 v[244:247], v145
	s_mov_b32 m0, s83
	v_lshl_add_u64 v[254:255], v[252:253], 0, s[38:39]
	global_load_lds_dwordx4 v[254:255], off
	s_barrier
	s_waitcnt lgkmcnt(0)
	v_mfma_f32_16x16x32_f16 v[14:17], v[196:199], v[232:235], v[14:17]
	v_mfma_f32_16x16x32_f16 v[22:25], v[196:199], v[240:243], v[22:25]
	v_mfma_f32_16x16x32_f16 v[34:37], v[204:207], v[232:235], v[34:37]
	v_mfma_f32_16x16x32_f16 v[46:49], v[204:207], v[240:243], v[46:49]
	v_mfma_f32_16x16x32_f16 v[58:61], v[216:219], v[232:235], v[58:61]
	v_mfma_f32_16x16x32_f16 v[70:73], v[216:219], v[240:243], v[70:73]
	v_mfma_f32_16x16x32_f16 v[78:81], v[224:227], v[232:235], v[78:81]
	v_mfma_f32_16x16x32_f16 v[86:89], v[224:227], v[240:243], v[86:89]
	v_mfma_f32_16x16x32_f16 v[14:17], v[200:203], v[236:239], v[14:17]
	v_mfma_f32_16x16x32_f16 v[22:25], v[200:203], v[244:247], v[22:25]
	v_mfma_f32_16x16x32_f16 v[34:37], v[212:215], v[236:239], v[34:37]
	v_mfma_f32_16x16x32_f16 v[46:49], v[212:215], v[244:247], v[46:49]
	v_mfma_f32_16x16x32_f16 v[58:61], v[220:223], v[236:239], v[58:61]
	v_mfma_f32_16x16x32_f16 v[70:73], v[220:223], v[244:247], v[70:73]
	v_mfma_f32_16x16x32_f16 v[78:81], v[228:231], v[236:239], v[78:81]
	v_mfma_f32_16x16x32_f16 v[86:89], v[228:231], v[244:247], v[86:89]
	v_lshl_add_u64 v[192:193], v[192:193], 0, s[38:39]
	s_mov_b32 m0, s84
	s_barrier
	ds_read_b128 v[196:199], v173 offset:49152
	ds_read_b128 v[200:203], v173 offset:50176
	ds_read_b128 v[204:207], v173 offset:51200
	ds_read_b128 v[212:215], v173 offset:52224
	ds_read_b128 v[216:219], v173 offset:53248
	ds_read_b128 v[220:223], v173 offset:54272
	ds_read_b128 v[224:227], v173 offset:55296
	ds_read_b128 v[228:231], v173 offset:56320
	global_load_lds_dwordx4 v[192:193], off
	s_mov_b32 m0, s85
	v_lshl_add_u64 v[192:193], v[248:249], 0, s[38:39]
	global_load_lds_dwordx4 v[192:193], off
	s_barrier
	s_waitcnt lgkmcnt(0)
	v_mfma_f32_16x16x32_f16 v[26:29], v[196:199], v[176:179], v[26:29]
	v_mfma_f32_16x16x32_f16 v[38:41], v[196:199], v[184:187], v[38:41]
	v_mfma_f32_16x16x32_f16 v[50:53], v[204:207], v[176:179], v[50:53]
	v_mfma_f32_16x16x32_f16 v[62:65], v[204:207], v[184:187], v[62:65]
	v_mfma_f32_16x16x32_f16 v[74:77], v[216:219], v[176:179], v[74:77]
	v_mfma_f32_16x16x32_f16 v[82:85], v[216:219], v[184:187], v[82:85]
	v_mfma_f32_16x16x32_f16 v[90:93], v[224:227], v[176:179], v[90:93]
	v_mfma_f32_16x16x32_f16 v[94:97], v[224:227], v[184:187], v[94:97]
	v_mfma_f32_16x16x32_f16 v[26:29], v[200:203], v[180:183], v[26:29]
	v_mfma_f32_16x16x32_f16 v[38:41], v[200:203], v[188:191], v[38:41]
	v_mfma_f32_16x16x32_f16 v[50:53], v[212:215], v[180:183], v[50:53]
	v_mfma_f32_16x16x32_f16 v[62:65], v[212:215], v[188:191], v[62:65]
	v_mfma_f32_16x16x32_f16 v[74:77], v[220:223], v[180:183], v[74:77]
	v_mfma_f32_16x16x32_f16 v[82:85], v[220:223], v[188:191], v[82:85]
	v_mfma_f32_16x16x32_f16 v[90:93], v[228:231], v[180:183], v[90:93]
	v_mfma_f32_16x16x32_f16 v[94:97], v[228:231], v[188:191], v[94:97]
	s_barrier
	s_mov_b32 m0, s86
	v_lshl_add_u64 v[176:177], v[250:251], 0, s[40:41]
	global_load_lds_dwordx4 v[176:177], off
	s_mov_b32 m0, s87
	v_lshl_add_u64 v[176:177], v[252:253], 0, s[40:41]
	global_load_lds_dwordx4 v[176:177], off
	s_waitcnt vmcnt(6)
	s_barrier
	v_mfma_f32_16x16x32_f16 v[98:101], v[196:199], v[232:235], v[98:101]
	v_mfma_f32_16x16x32_f16 v[102:105], v[196:199], v[240:243], v[102:105]
	v_mfma_f32_16x16x32_f16 v[106:109], v[204:207], v[232:235], v[106:109]
	v_mfma_f32_16x16x32_f16 v[110:113], v[204:207], v[240:243], v[110:113]
	v_mfma_f32_16x16x32_f16 v[114:117], v[216:219], v[232:235], v[114:117]
	v_mfma_f32_16x16x32_f16 v[118:121], v[216:219], v[240:243], v[118:121]
	v_mfma_f32_16x16x32_f16 v[122:125], v[224:227], v[232:235], v[122:125]
	v_mfma_f32_16x16x32_f16 v[126:129], v[224:227], v[240:243], v[126:129]
	v_mfma_f32_16x16x32_f16 v[98:101], v[200:203], v[236:239], v[98:101]
	v_mfma_f32_16x16x32_f16 v[102:105], v[200:203], v[244:247], v[102:105]
	v_mfma_f32_16x16x32_f16 v[106:109], v[212:215], v[236:239], v[106:109]
	v_mfma_f32_16x16x32_f16 v[110:113], v[212:215], v[244:247], v[110:113]
	v_mfma_f32_16x16x32_f16 v[114:117], v[220:223], v[236:239], v[114:117]
	v_mfma_f32_16x16x32_f16 v[118:121], v[220:223], v[244:247], v[118:121]
	v_mfma_f32_16x16x32_f16 v[122:125], v[228:231], v[236:239], v[122:125]
	v_mfma_f32_16x16x32_f16 v[126:129], v[228:231], v[244:247], v[126:129]
	s_add_i32 s46, s46, 2
	s_add_u32 s44, s44, 0x100
	s_addc_u32 s45, s45, 0
	s_cmp_lt_u32 s46, 4
	s_barrier
	s_cbranch_scc1 .LBB6_12
	s_add_u32 s0, s0, 0x20380
	s_addc_u32 s1, s1, 0
	v_readfirstlane_b32 s17, v174
	v_lshl_add_u64 v[130:131], v[130:131], 1, s[0:1]
	s_mov_b32 m0, s17
	ds_read_b128 v[134:137], v169
	ds_read_b128 v[138:141], v170
	ds_read_b128 v[152:155], v171
	ds_read_b128 v[156:159], v172
	ds_read_b128 v[166:169], v173
	ds_read_b128 v[176:179], v173 offset:1024
	ds_read_b128 v[180:183], v173 offset:2048
	ds_read_b128 v[184:187], v173 offset:3072
	ds_read_b128 v[188:191], v173 offset:4096
	ds_read_b128 v[196:199], v173 offset:5120
	ds_read_b128 v[200:203], v173 offset:6144
	ds_read_b128 v[204:207], v173 offset:7168
	global_load_lds_dwordx4 v[130:131], off
	v_lshl_add_u64 v[130:131], v[132:133], 1, s[0:1]
	v_readfirstlane_b32 s0, v175
	s_mov_b32 m0, s0
	s_nop 0
	global_load_lds_dwordx4 v[130:131], off
	s_barrier
	s_waitcnt lgkmcnt(0)
	v_mfma_f32_16x16x32_f16 v[2:5], v[166:169], v[134:137], v[2:5]
	v_mfma_f32_16x16x32_f16 v[42:45], v[188:191], v[152:155], v[42:45]
	v_mfma_f32_16x16x32_f16 v[54:57], v[200:203], v[134:137], v[54:57]
	v_mfma_f32_16x16x32_f16 v[66:69], v[200:203], v[152:155], v[66:69]
	v_mfma_f32_16x16x32_f16 v[2:5], v[176:179], v[138:141], v[2:5]
	v_mfma_f32_16x16x32_f16 v[6:9], v[166:169], v[152:155], v[6:9]
	v_mfma_f32_16x16x32_f16 v[10:13], v[180:183], v[134:137], v[10:13]
	v_mfma_f32_16x16x32_f16 v[18:21], v[180:183], v[152:155], v[18:21]
	v_mfma_f32_16x16x32_f16 v[30:33], v[188:191], v[134:137], v[30:33]
	v_mfma_f32_16x16x32_f16 v[42:45], v[196:199], v[156:159], v[42:45]
	v_mfma_f32_16x16x32_f16 v[54:57], v[204:207], v[138:141], v[54:57]
	v_mfma_f32_16x16x32_f16 v[66:69], v[204:207], v[156:159], v[66:69]
	v_mfma_f32_16x16x32_f16 v[6:9], v[176:179], v[156:159], v[6:9]
	v_mfma_f32_16x16x32_f16 v[10:13], v[184:187], v[138:141], v[10:13]
	v_mfma_f32_16x16x32_f16 v[18:21], v[184:187], v[156:159], v[18:21]
	v_mfma_f32_16x16x32_f16 v[30:33], v[196:199], v[138:141], v[30:33]
	s_barrier
	ds_read_b128 v[130:133], v161
	ds_read_b128 v[212:215], v162
	ds_read_b128 v[160:163], v163
	ds_read_b128 v[216:219], v164
	s_barrier
	s_waitcnt lgkmcnt(0)
	v_mfma_f32_16x16x32_f16 v[14:17], v[166:169], v[130:133], v[14:17]
	v_mfma_f32_16x16x32_f16 v[78:81], v[200:203], v[130:133], v[78:81]
	v_mfma_f32_16x16x32_f16 v[14:17], v[176:179], v[212:215], v[14:17]
	v_mfma_f32_16x16x32_f16 v[22:25], v[166:169], v[160:163], v[22:25]
	v_mfma_f32_16x16x32_f16 v[34:37], v[180:183], v[130:133], v[34:37]
	v_mfma_f32_16x16x32_f16 v[46:49], v[180:183], v[160:163], v[46:49]
	v_mfma_f32_16x16x32_f16 v[58:61], v[188:191], v[130:133], v[58:61]
	v_mfma_f32_16x16x32_f16 v[70:73], v[188:191], v[160:163], v[70:73]
	v_mfma_f32_16x16x32_f16 v[164:167], v[204:207], v[212:215], v[78:81]
	v_mfma_f32_16x16x32_f16 v[78:81], v[200:203], v[160:163], v[86:89]
	v_mfma_f32_16x16x32_f16 v[22:25], v[176:179], v[216:219], v[22:25]
	v_mfma_f32_16x16x32_f16 v[34:37], v[184:187], v[212:215], v[34:37]
	v_mfma_f32_16x16x32_f16 v[46:49], v[184:187], v[216:219], v[46:49]
	v_mfma_f32_16x16x32_f16 v[58:61], v[196:199], v[212:215], v[58:61]
	v_mfma_f32_16x16x32_f16 v[70:73], v[196:199], v[216:219], v[70:73]
	v_mfma_f32_16x16x32_f16 v[86:89], v[204:207], v[216:219], v[78:81]
	s_barrier
	s_nop 0
	ds_read_b128 v[78:81], v173 offset:16384
	ds_read_b128 v[168:171], v173 offset:17408
	ds_read_b128 v[174:177], v173 offset:18432
	ds_read_b128 v[178:181], v173 offset:19456
	ds_read_b128 v[182:185], v173 offset:20480
	ds_read_b128 v[186:189], v173 offset:21504
	ds_read_b128 v[190:193], v173 offset:22528
	ds_read_b128 v[196:199], v173 offset:23552
	s_waitcnt vmcnt(4)
	s_barrier
	s_waitcnt lgkmcnt(0)
	v_mfma_f32_16x16x32_f16 v[26:29], v[78:81], v[134:137], v[26:29]
	v_mfma_f32_16x16x32_f16 v[38:41], v[78:81], v[152:155], v[38:41]
	v_mfma_f32_16x16x32_f16 v[26:29], v[168:171], v[138:141], v[26:29]
	v_mfma_f32_16x16x32_f16 v[38:41], v[168:171], v[156:159], v[38:41]
	v_mfma_f32_16x16x32_f16 v[50:53], v[174:177], v[134:137], v[50:53]
	v_mfma_f32_16x16x32_f16 v[62:65], v[174:177], v[152:155], v[62:65]
	v_mfma_f32_16x16x32_f16 v[74:77], v[182:185], v[134:137], v[74:77]
	v_mfma_f32_16x16x32_f16 v[82:85], v[182:185], v[152:155], v[82:85]
	v_mfma_f32_16x16x32_f16 v[90:93], v[190:193], v[134:137], v[90:93]
	v_mfma_f32_16x16x32_f16 v[94:97], v[190:193], v[152:155], v[94:97]
	v_mfma_f32_16x16x32_f16 v[50:53], v[178:181], v[138:141], v[50:53]
	v_mfma_f32_16x16x32_f16 v[62:65], v[178:181], v[156:159], v[62:65]
	v_mfma_f32_16x16x32_f16 v[74:77], v[186:189], v[138:141], v[74:77]
	v_mfma_f32_16x16x32_f16 v[82:85], v[186:189], v[156:159], v[82:85]
	v_mfma_f32_16x16x32_f16 v[90:93], v[196:199], v[138:141], v[90:93]
	v_mfma_f32_16x16x32_f16 v[94:97], v[196:199], v[156:159], v[94:97]
	v_mfma_f32_16x16x32_f16 v[98:101], v[78:81], v[130:133], v[98:101]
	v_mfma_f32_16x16x32_f16 v[78:81], v[78:81], v[160:163], v[102:105]
	v_mfma_f32_16x16x32_f16 v[102:105], v[168:171], v[216:219], v[78:81]
	v_mfma_f32_16x16x32_f16 v[78:81], v[174:177], v[130:133], v[106:109]
	v_mfma_f32_16x16x32_f16 v[106:109], v[178:181], v[212:215], v[78:81]
	v_mfma_f32_16x16x32_f16 v[78:81], v[174:177], v[160:163], v[110:113]
	v_mfma_f32_16x16x32_f16 v[200:203], v[178:181], v[216:219], v[78:81]
	v_mfma_f32_16x16x32_f16 v[78:81], v[182:185], v[130:133], v[114:117]
	v_mfma_f32_16x16x32_f16 v[204:207], v[186:189], v[212:215], v[78:81]
	v_mfma_f32_16x16x32_f16 v[78:81], v[182:185], v[160:163], v[118:121]
	v_mfma_f32_16x16x32_f16 v[220:223], v[186:189], v[216:219], v[78:81]
	v_mfma_f32_16x16x32_f16 v[78:81], v[190:193], v[130:133], v[122:125]
	v_mfma_f32_16x16x32_f16 v[98:101], v[168:171], v[212:215], v[98:101]
	v_mfma_f32_16x16x32_f16 v[212:215], v[196:199], v[212:215], v[78:81]
	v_mfma_f32_16x16x32_f16 v[78:81], v[190:193], v[160:163], v[126:129]
	v_mfma_f32_16x16x32_f16 v[196:199], v[196:199], v[216:219], v[78:81]
	s_barrier
	ds_read_b128 v[110:113], v148
	ds_read_b128 v[130:133], v149
	ds_read_b128 v[216:219], v150
	ds_read_b128 v[224:227], v151
	s_nop 0
	ds_read_b128 v[78:81], v173 offset:32768
	ds_read_b128 v[114:117], v173 offset:33792
	ds_read_b128 v[118:121], v173 offset:34816
	ds_read_b128 v[134:137], v173 offset:35840
	ds_read_b128 v[138:141], v173 offset:36864
	ds_read_b128 v[168:171], v173 offset:37888
	ds_read_b128 v[174:177], v173 offset:38912
	ds_read_b128 v[228:231], v173 offset:39936
	s_waitcnt vmcnt(2)
	s_barrier
	s_waitcnt lgkmcnt(0)
	v_mfma_f32_16x16x32_f16 v[2:5], v[78:81], v[110:113], v[2:5]
	v_mfma_f32_16x16x32_f16 v[190:193], v[114:117], v[130:133], v[2:5]
	v_mfma_f32_16x16x32_f16 v[2:5], v[78:81], v[216:219], v[6:9]
	v_mfma_f32_16x16x32_f16 v[158:161], v[114:117], v[224:227], v[2:5]
	v_mfma_f32_16x16x32_f16 v[2:5], v[118:121], v[110:113], v[10:13]
	v_mfma_f32_16x16x32_f16 v[186:189], v[134:137], v[130:133], v[2:5]
	v_mfma_f32_16x16x32_f16 v[2:5], v[118:121], v[216:219], v[18:21]
	v_mfma_f32_16x16x32_f16 v[154:157], v[134:137], v[224:227], v[2:5]
	v_mfma_f32_16x16x32_f16 v[2:5], v[138:141], v[110:113], v[30:33]
	v_mfma_f32_16x16x32_f16 v[182:185], v[168:171], v[130:133], v[2:5]
	v_mfma_f32_16x16x32_f16 v[2:5], v[138:141], v[216:219], v[42:45]
	v_mfma_f32_16x16x32_f16 v[150:153], v[168:171], v[224:227], v[2:5]
	v_mfma_f32_16x16x32_f16 v[2:5], v[174:177], v[110:113], v[54:57]
	v_mfma_f32_16x16x32_f16 v[178:181], v[228:231], v[130:133], v[2:5]
	v_mfma_f32_16x16x32_f16 v[2:5], v[174:177], v[216:219], v[66:69]
	v_mfma_f32_16x16x32_f16 v[146:149], v[228:231], v[224:227], v[2:5]
	s_barrier
	s_nop 4
	ds_read_b128 v[2:5], v142
	ds_read_b128 v[6:9], v143
	ds_read_b128 v[10:13], v144
	ds_read_b128 v[18:21], v145
	s_waitcnt vmcnt(0)
	s_barrier
	s_waitcnt lgkmcnt(0)
	v_mfma_f32_16x16x32_f16 v[14:17], v[78:81], v[2:5], v[14:17]
	v_mfma_f32_16x16x32_f16 v[126:129], v[114:117], v[6:9], v[14:17]
	v_mfma_f32_16x16x32_f16 v[14:17], v[78:81], v[10:13], v[22:25]
	v_mfma_f32_16x16x32_f16 v[78:81], v[114:117], v[18:21], v[14:17]
	v_mfma_f32_16x16x32_f16 v[14:17], v[118:121], v[2:5], v[34:37]
	v_mfma_f32_16x16x32_f16 v[122:125], v[134:137], v[6:9], v[14:17]
	v_mfma_f32_16x16x32_f16 v[14:17], v[118:121], v[10:13], v[46:49]
	v_mfma_f32_16x16x32_f16 v[66:69], v[134:137], v[18:21], v[14:17]
	v_mfma_f32_16x16x32_f16 v[14:17], v[138:141], v[2:5], v[58:61]
	v_mfma_f32_16x16x32_f16 v[118:121], v[168:171], v[6:9], v[14:17]
	v_mfma_f32_16x16x32_f16 v[14:17], v[138:141], v[10:13], v[70:73]
	v_mfma_f32_16x16x32_f16 v[54:57], v[168:171], v[18:21], v[14:17]
	v_mfma_f32_16x16x32_f16 v[14:17], v[174:177], v[2:5], v[164:167]
	v_mfma_f32_16x16x32_f16 v[114:117], v[228:231], v[6:9], v[14:17]
	v_mfma_f32_16x16x32_f16 v[14:17], v[174:177], v[10:13], v[86:89]
	v_mfma_f32_16x16x32_f16 v[42:45], v[228:231], v[18:21], v[14:17]
	s_barrier
	s_nop 4
	ds_read_b128 v[14:17], v173 offset:49152
	ds_read_b128 v[22:25], v173 offset:50176
	ds_read_b128 v[30:33], v173 offset:51200
	ds_read_b128 v[34:37], v173 offset:52224
	ds_read_b128 v[46:49], v173 offset:53248
	ds_read_b128 v[58:61], v173 offset:54272
	ds_read_b128 v[70:73], v173 offset:55296
	ds_read_b128 v[86:89], v173 offset:56320
	s_barrier
	s_waitcnt lgkmcnt(0)
	v_mfma_f32_16x16x32_f16 v[26:29], v[14:17], v[110:113], v[26:29]
	v_mfma_f32_16x16x32_f16 v[174:177], v[22:25], v[130:133], v[26:29]
	v_mfma_f32_16x16x32_f16 v[26:29], v[14:17], v[216:219], v[38:41]
	v_mfma_f32_16x16x32_f16 v[142:145], v[22:25], v[224:227], v[26:29]
	v_mfma_f32_16x16x32_f16 v[26:29], v[30:33], v[110:113], v[50:53]
	v_mfma_f32_16x16x32_f16 v[170:173], v[34:37], v[130:133], v[26:29]
	v_mfma_f32_16x16x32_f16 v[26:29], v[30:33], v[216:219], v[62:65]
	v_mfma_f32_16x16x32_f16 v[138:141], v[34:37], v[224:227], v[26:29]
	v_mfma_f32_16x16x32_f16 v[26:29], v[46:49], v[110:113], v[74:77]
	v_mfma_f32_16x16x32_f16 v[166:169], v[58:61], v[130:133], v[26:29]
	v_mfma_f32_16x16x32_f16 v[26:29], v[46:49], v[216:219], v[82:85]
	v_mfma_f32_16x16x32_f16 v[134:137], v[58:61], v[224:227], v[26:29]
	v_mfma_f32_16x16x32_f16 v[26:29], v[70:73], v[110:113], v[90:93]
	v_mfma_f32_16x16x32_f16 v[162:165], v[86:89], v[130:133], v[26:29]
	v_mfma_f32_16x16x32_f16 v[26:29], v[70:73], v[216:219], v[94:97]
	v_mfma_f32_16x16x32_f16 v[130:133], v[86:89], v[224:227], v[26:29]
	v_mfma_f32_16x16x32_f16 v[26:29], v[14:17], v[2:5], v[98:101]
	v_mfma_f32_16x16x32_f16 v[14:17], v[14:17], v[10:13], v[102:105]
	v_mfma_f32_16x16x32_f16 v[38:41], v[22:25], v[18:21], v[14:17]
	v_mfma_f32_16x16x32_f16 v[14:17], v[30:33], v[2:5], v[106:109]
	v_mfma_f32_16x16x32_f16 v[106:109], v[34:37], v[6:9], v[14:17]
	v_mfma_f32_16x16x32_f16 v[14:17], v[30:33], v[10:13], v[200:203]
	v_mfma_f32_16x16x32_f16 v[110:113], v[22:25], v[6:9], v[26:29]
	v_mfma_f32_16x16x32_f16 v[26:29], v[34:37], v[18:21], v[14:17]
	v_mfma_f32_16x16x32_f16 v[14:17], v[46:49], v[2:5], v[204:207]
	v_mfma_f32_16x16x32_f16 v[2:5], v[70:73], v[2:5], v[212:215]
	v_mfma_f32_16x16x32_f16 v[102:105], v[58:61], v[6:9], v[14:17]
	v_mfma_f32_16x16x32_f16 v[14:17], v[46:49], v[10:13], v[220:223]
	v_mfma_f32_16x16x32_f16 v[98:101], v[86:89], v[6:9], v[2:5]
	v_mfma_f32_16x16x32_f16 v[2:5], v[70:73], v[10:13], v[196:199]
	v_mfma_f32_16x16x32_f16 v[14:17], v[58:61], v[18:21], v[14:17]
	v_mfma_f32_16x16x32_f16 v[2:5], v[86:89], v[18:21], v[2:5]
	s_cmpk_gt_u32 s65, 0xff
	s_barrier
	s_cbranch_scc1 .LBB6_15
	s_barrier

.LBB7_239:
	ds_read_b128 v[176:179], v169
	ds_read_b128 v[180:183], v170
	ds_read_b128 v[184:187], v171
	ds_read_b128 v[188:191], v172
	v_add_u32_e32 v174, 0xc000, v152
	v_lshl_add_u64 v[192:193], v[136:137], 0, s[46:47]
	v_add_u32_e32 v175, 0xe000, v152
	v_add_u32_e32 v173, s5, v168
	v_lshl_add_u64 v[232:233], v[192:193], 0, s[34:35]
	s_mov_b32 m0, s72
	v_lshl_add_u64 v[248:249], v[134:135], 0, s[46:47]
	ds_read_b128 v[196:199], v173
	ds_read_b128 v[200:203], v173 offset:1024
	ds_read_b128 v[204:207], v173 offset:2048
	ds_read_b128 v[212:215], v173 offset:3072
	ds_read_b128 v[216:219], v173 offset:4096
	ds_read_b128 v[220:223], v173 offset:5120
	ds_read_b128 v[224:227], v173 offset:6144
	ds_read_b128 v[228:231], v173 offset:7168
	global_load_lds_dwordx4 v[232:233], off
	s_mov_b32 m0, s73
	v_lshl_add_u64 v[232:233], v[248:249], 0, s[34:35]
	global_load_lds_dwordx4 v[232:233], off
	s_waitcnt lgkmcnt(8)
	s_barrier
	s_waitcnt lgkmcnt(0)
	v_mfma_f32_16x16x32_f16 v[2:5], v[196:199], v[176:179], v[2:5]
	v_mfma_f32_16x16x32_f16 v[6:9], v[196:199], v[184:187], v[6:9]
	v_mfma_f32_16x16x32_f16 v[10:13], v[204:207], v[176:179], v[10:13]
	v_mfma_f32_16x16x32_f16 v[18:21], v[204:207], v[184:187], v[18:21]
	v_mfma_f32_16x16x32_f16 v[30:33], v[216:219], v[176:179], v[30:33]
	v_mfma_f32_16x16x32_f16 v[42:45], v[216:219], v[184:187], v[42:45]
	v_mfma_f32_16x16x32_f16 v[54:57], v[224:227], v[176:179], v[54:57]
	v_mfma_f32_16x16x32_f16 v[66:69], v[224:227], v[184:187], v[66:69]
	v_mfma_f32_16x16x32_f16 v[2:5], v[200:203], v[180:183], v[2:5]
	v_mfma_f32_16x16x32_f16 v[6:9], v[200:203], v[188:191], v[6:9]
	v_mfma_f32_16x16x32_f16 v[10:13], v[212:215], v[180:183], v[10:13]
	v_mfma_f32_16x16x32_f16 v[18:21], v[212:215], v[188:191], v[18:21]
	v_mfma_f32_16x16x32_f16 v[30:33], v[220:223], v[180:183], v[30:33]
	v_mfma_f32_16x16x32_f16 v[42:45], v[220:223], v[188:191], v[42:45]
	v_mfma_f32_16x16x32_f16 v[54:57], v[228:231], v[180:183], v[54:57]
	v_mfma_f32_16x16x32_f16 v[66:69], v[228:231], v[188:191], v[66:69]
	s_barrier
	v_lshl_add_u64 v[250:251], v[140:141], 0, s[46:47]
	s_mov_b32 m0, s74
	v_lshl_add_u64 v[252:253], v[250:251], 0, s[36:37]
	global_load_lds_dwordx4 v[252:253], off
	ds_read_b128 v[232:235], v161
	ds_read_b128 v[236:239], v162
	ds_read_b128 v[240:243], v163
	ds_read_b128 v[244:247], v164
	v_lshl_add_u64 v[252:253], v[138:139], 0, s[46:47]
	s_mov_b32 m0, s75
	v_lshl_add_u64 v[254:255], v[252:253], 0, s[36:37]
	global_load_lds_dwordx4 v[254:255], off
	s_barrier
	s_waitcnt lgkmcnt(0)
	v_mfma_f32_16x16x32_f16 v[14:17], v[196:199], v[232:235], v[14:17]
	v_mfma_f32_16x16x32_f16 v[22:25], v[196:199], v[240:243], v[22:25]
	v_mfma_f32_16x16x32_f16 v[34:37], v[204:207], v[232:235], v[34:37]
	v_mfma_f32_16x16x32_f16 v[46:49], v[204:207], v[240:243], v[46:49]
	v_mfma_f32_16x16x32_f16 v[58:61], v[216:219], v[232:235], v[58:61]
	v_mfma_f32_16x16x32_f16 v[70:73], v[216:219], v[240:243], v[70:73]
	v_mfma_f32_16x16x32_f16 v[78:81], v[224:227], v[232:235], v[78:81]
	v_mfma_f32_16x16x32_f16 v[86:89], v[224:227], v[240:243], v[86:89]
	v_mfma_f32_16x16x32_f16 v[14:17], v[200:203], v[236:239], v[14:17]
	v_mfma_f32_16x16x32_f16 v[22:25], v[200:203], v[244:247], v[22:25]
	v_mfma_f32_16x16x32_f16 v[34:37], v[212:215], v[236:239], v[34:37]
	v_mfma_f32_16x16x32_f16 v[46:49], v[212:215], v[244:247], v[46:49]
	v_mfma_f32_16x16x32_f16 v[58:61], v[220:223], v[236:239], v[58:61]
	v_mfma_f32_16x16x32_f16 v[70:73], v[220:223], v[244:247], v[70:73]
	v_mfma_f32_16x16x32_f16 v[78:81], v[228:231], v[236:239], v[78:81]
	v_mfma_f32_16x16x32_f16 v[86:89], v[228:231], v[244:247], v[86:89]
	v_lshl_add_u64 v[254:255], v[192:193], 0, s[36:37]
	s_mov_b32 m0, s76
	s_barrier
	ds_read_b128 v[196:199], v173 offset:16384
	ds_read_b128 v[200:203], v173 offset:17408
	ds_read_b128 v[204:207], v173 offset:18432
	ds_read_b128 v[212:215], v173 offset:19456
	ds_read_b128 v[216:219], v173 offset:20480
	ds_read_b128 v[220:223], v173 offset:21504
	ds_read_b128 v[224:227], v173 offset:22528
	ds_read_b128 v[228:231], v173 offset:23552
	global_load_lds_dwordx4 v[254:255], off
	s_mov_b32 m0, s77
	v_lshl_add_u64 v[254:255], v[248:249], 0, s[36:37]
	global_load_lds_dwordx4 v[254:255], off
	s_barrier
	s_waitcnt lgkmcnt(0)
	v_mfma_f32_16x16x32_f16 v[26:29], v[196:199], v[176:179], v[26:29]
	v_mfma_f32_16x16x32_f16 v[38:41], v[196:199], v[184:187], v[38:41]
	v_mfma_f32_16x16x32_f16 v[50:53], v[204:207], v[176:179], v[50:53]
	v_mfma_f32_16x16x32_f16 v[62:65], v[204:207], v[184:187], v[62:65]
	v_mfma_f32_16x16x32_f16 v[74:77], v[216:219], v[176:179], v[74:77]
	v_mfma_f32_16x16x32_f16 v[82:85], v[216:219], v[184:187], v[82:85]
	v_mfma_f32_16x16x32_f16 v[90:93], v[224:227], v[176:179], v[90:93]
	v_mfma_f32_16x16x32_f16 v[94:97], v[224:227], v[184:187], v[94:97]
	v_mfma_f32_16x16x32_f16 v[26:29], v[200:203], v[180:183], v[26:29]
	v_mfma_f32_16x16x32_f16 v[38:41], v[200:203], v[188:191], v[38:41]
	v_mfma_f32_16x16x32_f16 v[50:53], v[212:215], v[180:183], v[50:53]
	v_mfma_f32_16x16x32_f16 v[62:65], v[212:215], v[188:191], v[62:65]
	v_mfma_f32_16x16x32_f16 v[74:77], v[220:223], v[180:183], v[74:77]
	v_mfma_f32_16x16x32_f16 v[82:85], v[220:223], v[188:191], v[82:85]
	v_mfma_f32_16x16x32_f16 v[90:93], v[228:231], v[180:183], v[90:93]
	v_mfma_f32_16x16x32_f16 v[94:97], v[228:231], v[188:191], v[94:97]
	s_barrier
	s_mov_b32 m0, s78
	v_lshl_add_u64 v[176:177], v[250:251], 0, s[38:39]
	global_load_lds_dwordx4 v[176:177], off
	s_mov_b32 m0, s79
	v_lshl_add_u64 v[176:177], v[252:253], 0, s[38:39]
	global_load_lds_dwordx4 v[176:177], off
	s_waitcnt vmcnt(6)
	s_barrier
	v_mfma_f32_16x16x32_f16 v[98:101], v[196:199], v[232:235], v[98:101]
	v_mfma_f32_16x16x32_f16 v[102:105], v[196:199], v[240:243], v[102:105]
	v_mfma_f32_16x16x32_f16 v[106:109], v[204:207], v[232:235], v[106:109]
	v_mfma_f32_16x16x32_f16 v[110:113], v[204:207], v[240:243], v[110:113]
	v_mfma_f32_16x16x32_f16 v[114:117], v[216:219], v[232:235], v[114:117]
	v_mfma_f32_16x16x32_f16 v[118:121], v[216:219], v[240:243], v[118:121]
	v_mfma_f32_16x16x32_f16 v[122:125], v[224:227], v[232:235], v[122:125]
	v_mfma_f32_16x16x32_f16 v[126:129], v[224:227], v[240:243], v[126:129]
	v_mfma_f32_16x16x32_f16 v[98:101], v[200:203], v[236:239], v[98:101]
	v_mfma_f32_16x16x32_f16 v[102:105], v[200:203], v[244:247], v[102:105]
	v_mfma_f32_16x16x32_f16 v[106:109], v[212:215], v[236:239], v[106:109]
	v_mfma_f32_16x16x32_f16 v[110:113], v[212:215], v[244:247], v[110:113]
	v_mfma_f32_16x16x32_f16 v[114:117], v[220:223], v[236:239], v[114:117]
	v_mfma_f32_16x16x32_f16 v[118:121], v[220:223], v[244:247], v[118:121]
	v_mfma_f32_16x16x32_f16 v[122:125], v[228:231], v[236:239], v[122:125]
	v_mfma_f32_16x16x32_f16 v[126:129], v[228:231], v[244:247], v[126:129]
	s_barrier
	ds_read_b128 v[176:179], v148
	ds_read_b128 v[180:183], v149
	ds_read_b128 v[184:187], v150
	ds_read_b128 v[188:191], v151
	s_mov_b32 m0, s80
	v_lshl_add_u64 v[232:233], v[192:193], 0, s[38:39]
	global_load_lds_dwordx4 v[232:233], off
	ds_read_b128 v[196:199], v173 offset:32768
	ds_read_b128 v[200:203], v173 offset:33792
	ds_read_b128 v[204:207], v173 offset:34816
	ds_read_b128 v[212:215], v173 offset:35840
	ds_read_b128 v[216:219], v173 offset:36864
	ds_read_b128 v[220:223], v173 offset:37888
	ds_read_b128 v[224:227], v173 offset:38912
	ds_read_b128 v[228:231], v173 offset:39936
	s_mov_b32 m0, s81
	v_lshl_add_u64 v[232:233], v[248:249], 0, s[38:39]
	global_load_lds_dwordx4 v[232:233], off
	s_waitcnt lgkmcnt(8)
	s_barrier
	s_waitcnt lgkmcnt(0)
	v_mfma_f32_16x16x32_f16 v[2:5], v[196:199], v[176:179], v[2:5]
	v_mfma_f32_16x16x32_f16 v[6:9], v[196:199], v[184:187], v[6:9]
	v_mfma_f32_16x16x32_f16 v[10:13], v[204:207], v[176:179], v[10:13]
	v_mfma_f32_16x16x32_f16 v[18:21], v[204:207], v[184:187], v[18:21]
	v_mfma_f32_16x16x32_f16 v[30:33], v[216:219], v[176:179], v[30:33]
	v_mfma_f32_16x16x32_f16 v[42:45], v[216:219], v[184:187], v[42:45]
	v_mfma_f32_16x16x32_f16 v[54:57], v[224:227], v[176:179], v[54:57]
	v_mfma_f32_16x16x32_f16 v[66:69], v[224:227], v[184:187], v[66:69]
	v_mfma_f32_16x16x32_f16 v[2:5], v[200:203], v[180:183], v[2:5]
	v_mfma_f32_16x16x32_f16 v[6:9], v[200:203], v[188:191], v[6:9]
	v_mfma_f32_16x16x32_f16 v[10:13], v[212:215], v[180:183], v[10:13]
	v_mfma_f32_16x16x32_f16 v[18:21], v[212:215], v[188:191], v[18:21]
	v_mfma_f32_16x16x32_f16 v[30:33], v[220:223], v[180:183], v[30:33]
	v_mfma_f32_16x16x32_f16 v[42:45], v[220:223], v[188:191], v[42:45]
	v_mfma_f32_16x16x32_f16 v[54:57], v[228:231], v[180:183], v[54:57]
	v_mfma_f32_16x16x32_f16 v[66:69], v[228:231], v[188:191], v[66:69]
	s_barrier
	s_mov_b32 m0, s82
	v_lshl_add_u64 v[254:255], v[250:251], 0, s[40:41]
	global_load_lds_dwordx4 v[254:255], off
	ds_read_b128 v[232:235], v142
	ds_read_b128 v[236:239], v143
	ds_read_b128 v[240:243], v144
	ds_read_b128 v[244:247], v145
	s_mov_b32 m0, s83
	v_lshl_add_u64 v[254:255], v[252:253], 0, s[40:41]
	global_load_lds_dwordx4 v[254:255], off
	s_barrier
	s_waitcnt lgkmcnt(0)
	v_mfma_f32_16x16x32_f16 v[14:17], v[196:199], v[232:235], v[14:17]
	v_mfma_f32_16x16x32_f16 v[22:25], v[196:199], v[240:243], v[22:25]
	v_mfma_f32_16x16x32_f16 v[34:37], v[204:207], v[232:235], v[34:37]
	v_mfma_f32_16x16x32_f16 v[46:49], v[204:207], v[240:243], v[46:49]
	v_mfma_f32_16x16x32_f16 v[58:61], v[216:219], v[232:235], v[58:61]
	v_mfma_f32_16x16x32_f16 v[70:73], v[216:219], v[240:243], v[70:73]
	v_mfma_f32_16x16x32_f16 v[78:81], v[224:227], v[232:235], v[78:81]
	v_mfma_f32_16x16x32_f16 v[86:89], v[224:227], v[240:243], v[86:89]
	v_mfma_f32_16x16x32_f16 v[14:17], v[200:203], v[236:239], v[14:17]
	v_mfma_f32_16x16x32_f16 v[22:25], v[200:203], v[244:247], v[22:25]
	v_mfma_f32_16x16x32_f16 v[34:37], v[212:215], v[236:239], v[34:37]
	v_mfma_f32_16x16x32_f16 v[46:49], v[212:215], v[244:247], v[46:49]
	v_mfma_f32_16x16x32_f16 v[58:61], v[220:223], v[236:239], v[58:61]
	v_mfma_f32_16x16x32_f16 v[70:73], v[220:223], v[244:247], v[70:73]
	v_mfma_f32_16x16x32_f16 v[78:81], v[228:231], v[236:239], v[78:81]
	v_mfma_f32_16x16x32_f16 v[86:89], v[228:231], v[244:247], v[86:89]
	v_lshl_add_u64 v[192:193], v[192:193], 0, s[40:41]
	s_mov_b32 m0, s84
	s_barrier
	ds_read_b128 v[196:199], v173 offset:49152
	ds_read_b128 v[200:203], v173 offset:50176
	ds_read_b128 v[204:207], v173 offset:51200
	ds_read_b128 v[212:215], v173 offset:52224
	ds_read_b128 v[216:219], v173 offset:53248
	ds_read_b128 v[220:223], v173 offset:54272
	ds_read_b128 v[224:227], v173 offset:55296
	ds_read_b128 v[228:231], v173 offset:56320
	global_load_lds_dwordx4 v[192:193], off
	s_mov_b32 m0, s85
	v_lshl_add_u64 v[192:193], v[248:249], 0, s[40:41]
	global_load_lds_dwordx4 v[192:193], off
	s_barrier
	s_waitcnt lgkmcnt(0)
	v_mfma_f32_16x16x32_f16 v[26:29], v[196:199], v[176:179], v[26:29]
	v_mfma_f32_16x16x32_f16 v[38:41], v[196:199], v[184:187], v[38:41]
	v_mfma_f32_16x16x32_f16 v[50:53], v[204:207], v[176:179], v[50:53]
	v_mfma_f32_16x16x32_f16 v[62:65], v[204:207], v[184:187], v[62:65]
	v_mfma_f32_16x16x32_f16 v[74:77], v[216:219], v[176:179], v[74:77]
	v_mfma_f32_16x16x32_f16 v[82:85], v[216:219], v[184:187], v[82:85]
	v_mfma_f32_16x16x32_f16 v[90:93], v[224:227], v[176:179], v[90:93]
	v_mfma_f32_16x16x32_f16 v[94:97], v[224:227], v[184:187], v[94:97]
	v_mfma_f32_16x16x32_f16 v[26:29], v[200:203], v[180:183], v[26:29]
	v_mfma_f32_16x16x32_f16 v[38:41], v[200:203], v[188:191], v[38:41]
	v_mfma_f32_16x16x32_f16 v[50:53], v[212:215], v[180:183], v[50:53]
	v_mfma_f32_16x16x32_f16 v[62:65], v[212:215], v[188:191], v[62:65]
	v_mfma_f32_16x16x32_f16 v[74:77], v[220:223], v[180:183], v[74:77]
	v_mfma_f32_16x16x32_f16 v[82:85], v[220:223], v[188:191], v[82:85]
	v_mfma_f32_16x16x32_f16 v[90:93], v[228:231], v[180:183], v[90:93]
	v_mfma_f32_16x16x32_f16 v[94:97], v[228:231], v[188:191], v[94:97]
	s_barrier
	s_mov_b32 m0, s86
	v_lshl_add_u64 v[176:177], v[250:251], 0, s[42:43]
	global_load_lds_dwordx4 v[176:177], off
	s_mov_b32 m0, s87
	v_lshl_add_u64 v[176:177], v[252:253], 0, s[42:43]
	global_load_lds_dwordx4 v[176:177], off
	s_waitcnt vmcnt(6)
	s_barrier
	v_mfma_f32_16x16x32_f16 v[98:101], v[196:199], v[232:235], v[98:101]
	v_mfma_f32_16x16x32_f16 v[102:105], v[196:199], v[240:243], v[102:105]
	v_mfma_f32_16x16x32_f16 v[106:109], v[204:207], v[232:235], v[106:109]
	v_mfma_f32_16x16x32_f16 v[110:113], v[204:207], v[240:243], v[110:113]
	v_mfma_f32_16x16x32_f16 v[114:117], v[216:219], v[232:235], v[114:117]
	v_mfma_f32_16x16x32_f16 v[118:121], v[216:219], v[240:243], v[118:121]
	v_mfma_f32_16x16x32_f16 v[122:125], v[224:227], v[232:235], v[122:125]
	v_mfma_f32_16x16x32_f16 v[126:129], v[224:227], v[240:243], v[126:129]
	v_mfma_f32_16x16x32_f16 v[98:101], v[200:203], v[236:239], v[98:101]
	v_mfma_f32_16x16x32_f16 v[102:105], v[200:203], v[244:247], v[102:105]
	v_mfma_f32_16x16x32_f16 v[106:109], v[212:215], v[236:239], v[106:109]
	v_mfma_f32_16x16x32_f16 v[110:113], v[212:215], v[244:247], v[110:113]
	v_mfma_f32_16x16x32_f16 v[114:117], v[220:223], v[236:239], v[114:117]
	v_mfma_f32_16x16x32_f16 v[118:121], v[220:223], v[244:247], v[118:121]
	v_mfma_f32_16x16x32_f16 v[122:125], v[228:231], v[236:239], v[122:125]
	v_mfma_f32_16x16x32_f16 v[126:129], v[228:231], v[244:247], v[126:129]
	s_add_i32 s48, s48, 2
	s_add_u32 s46, s46, 0x100
	s_addc_u32 s47, s47, 0
	s_cmp_lt_u32 s48, 4
	s_barrier
	s_cbranch_scc1 .LBB7_239
	s_add_u32 s0, s0, 0x20380
	s_addc_u32 s1, s1, 0
	v_readfirstlane_b32 s5, v174
	v_lshl_add_u64 v[130:131], v[130:131], 1, s[0:1]
	s_mov_b32 m0, s5
	ds_read_b128 v[134:137], v169
	ds_read_b128 v[138:141], v170
	ds_read_b128 v[152:155], v171
	ds_read_b128 v[156:159], v172
	ds_read_b128 v[166:169], v173
	ds_read_b128 v[176:179], v173 offset:1024
	ds_read_b128 v[180:183], v173 offset:2048
	ds_read_b128 v[184:187], v173 offset:3072
	ds_read_b128 v[188:191], v173 offset:4096
	ds_read_b128 v[196:199], v173 offset:5120
	ds_read_b128 v[200:203], v173 offset:6144
	ds_read_b128 v[204:207], v173 offset:7168
	global_load_lds_dwordx4 v[130:131], off
	v_lshl_add_u64 v[130:131], v[132:133], 1, s[0:1]
	v_readfirstlane_b32 s0, v175
	s_mov_b32 m0, s0
	s_nop 0
	global_load_lds_dwordx4 v[130:131], off
	s_barrier
	s_waitcnt lgkmcnt(0)
	v_mfma_f32_16x16x32_f16 v[2:5], v[166:169], v[134:137], v[2:5]
	v_mfma_f32_16x16x32_f16 v[42:45], v[188:191], v[152:155], v[42:45]
	v_mfma_f32_16x16x32_f16 v[54:57], v[200:203], v[134:137], v[54:57]
	v_mfma_f32_16x16x32_f16 v[66:69], v[200:203], v[152:155], v[66:69]
	v_mfma_f32_16x16x32_f16 v[2:5], v[176:179], v[138:141], v[2:5]
	v_mfma_f32_16x16x32_f16 v[6:9], v[166:169], v[152:155], v[6:9]
	v_mfma_f32_16x16x32_f16 v[10:13], v[180:183], v[134:137], v[10:13]
	v_mfma_f32_16x16x32_f16 v[18:21], v[180:183], v[152:155], v[18:21]
	v_mfma_f32_16x16x32_f16 v[30:33], v[188:191], v[134:137], v[30:33]
	v_mfma_f32_16x16x32_f16 v[42:45], v[196:199], v[156:159], v[42:45]
	v_mfma_f32_16x16x32_f16 v[54:57], v[204:207], v[138:141], v[54:57]
	v_mfma_f32_16x16x32_f16 v[66:69], v[204:207], v[156:159], v[66:69]
	v_mfma_f32_16x16x32_f16 v[6:9], v[176:179], v[156:159], v[6:9]
	v_mfma_f32_16x16x32_f16 v[10:13], v[184:187], v[138:141], v[10:13]
	v_mfma_f32_16x16x32_f16 v[18:21], v[184:187], v[156:159], v[18:21]
	v_mfma_f32_16x16x32_f16 v[30:33], v[196:199], v[138:141], v[30:33]
	s_barrier
	ds_read_b128 v[130:133], v161
	ds_read_b128 v[212:215], v162
	ds_read_b128 v[160:163], v163
	ds_read_b128 v[216:219], v164
	s_barrier
	s_waitcnt lgkmcnt(0)
	v_mfma_f32_16x16x32_f16 v[14:17], v[166:169], v[130:133], v[14:17]
	v_mfma_f32_16x16x32_f16 v[78:81], v[200:203], v[130:133], v[78:81]
	v_mfma_f32_16x16x32_f16 v[14:17], v[176:179], v[212:215], v[14:17]
	v_mfma_f32_16x16x32_f16 v[22:25], v[166:169], v[160:163], v[22:25]
	v_mfma_f32_16x16x32_f16 v[34:37], v[180:183], v[130:133], v[34:37]
	v_mfma_f32_16x16x32_f16 v[46:49], v[180:183], v[160:163], v[46:49]
	v_mfma_f32_16x16x32_f16 v[58:61], v[188:191], v[130:133], v[58:61]
	v_mfma_f32_16x16x32_f16 v[70:73], v[188:191], v[160:163], v[70:73]
	v_mfma_f32_16x16x32_f16 v[164:167], v[204:207], v[212:215], v[78:81]
	v_mfma_f32_16x16x32_f16 v[78:81], v[200:203], v[160:163], v[86:89]
	v_mfma_f32_16x16x32_f16 v[22:25], v[176:179], v[216:219], v[22:25]
	v_mfma_f32_16x16x32_f16 v[34:37], v[184:187], v[212:215], v[34:37]
	v_mfma_f32_16x16x32_f16 v[46:49], v[184:187], v[216:219], v[46:49]
	v_mfma_f32_16x16x32_f16 v[58:61], v[196:199], v[212:215], v[58:61]
	v_mfma_f32_16x16x32_f16 v[70:73], v[196:199], v[216:219], v[70:73]
	v_mfma_f32_16x16x32_f16 v[86:89], v[204:207], v[216:219], v[78:81]
	s_barrier
	s_nop 0
	ds_read_b128 v[78:81], v173 offset:16384
	ds_read_b128 v[168:171], v173 offset:17408
	ds_read_b128 v[174:177], v173 offset:18432
	ds_read_b128 v[178:181], v173 offset:19456
	ds_read_b128 v[182:185], v173 offset:20480
	ds_read_b128 v[186:189], v173 offset:21504
	ds_read_b128 v[190:193], v173 offset:22528
	ds_read_b128 v[196:199], v173 offset:23552
	s_waitcnt vmcnt(4)
	s_barrier
	s_waitcnt lgkmcnt(0)
	v_mfma_f32_16x16x32_f16 v[26:29], v[78:81], v[134:137], v[26:29]
	v_mfma_f32_16x16x32_f16 v[38:41], v[78:81], v[152:155], v[38:41]
	v_mfma_f32_16x16x32_f16 v[26:29], v[168:171], v[138:141], v[26:29]
	v_mfma_f32_16x16x32_f16 v[38:41], v[168:171], v[156:159], v[38:41]
	v_mfma_f32_16x16x32_f16 v[50:53], v[174:177], v[134:137], v[50:53]
	v_mfma_f32_16x16x32_f16 v[62:65], v[174:177], v[152:155], v[62:65]
	v_mfma_f32_16x16x32_f16 v[74:77], v[182:185], v[134:137], v[74:77]
	v_mfma_f32_16x16x32_f16 v[82:85], v[182:185], v[152:155], v[82:85]
	v_mfma_f32_16x16x32_f16 v[90:93], v[190:193], v[134:137], v[90:93]
	v_mfma_f32_16x16x32_f16 v[94:97], v[190:193], v[152:155], v[94:97]
	v_mfma_f32_16x16x32_f16 v[50:53], v[178:181], v[138:141], v[50:53]
	v_mfma_f32_16x16x32_f16 v[62:65], v[178:181], v[156:159], v[62:65]
	v_mfma_f32_16x16x32_f16 v[74:77], v[186:189], v[138:141], v[74:77]
	v_mfma_f32_16x16x32_f16 v[82:85], v[186:189], v[156:159], v[82:85]
	v_mfma_f32_16x16x32_f16 v[90:93], v[196:199], v[138:141], v[90:93]
	v_mfma_f32_16x16x32_f16 v[94:97], v[196:199], v[156:159], v[94:97]
	v_mfma_f32_16x16x32_f16 v[98:101], v[78:81], v[130:133], v[98:101]
	v_mfma_f32_16x16x32_f16 v[78:81], v[78:81], v[160:163], v[102:105]
	v_mfma_f32_16x16x32_f16 v[102:105], v[168:171], v[216:219], v[78:81]
	v_mfma_f32_16x16x32_f16 v[78:81], v[174:177], v[130:133], v[106:109]
	v_mfma_f32_16x16x32_f16 v[106:109], v[178:181], v[212:215], v[78:81]
	v_mfma_f32_16x16x32_f16 v[78:81], v[174:177], v[160:163], v[110:113]
	v_mfma_f32_16x16x32_f16 v[200:203], v[178:181], v[216:219], v[78:81]
	v_mfma_f32_16x16x32_f16 v[78:81], v[182:185], v[130:133], v[114:117]
	v_mfma_f32_16x16x32_f16 v[204:207], v[186:189], v[212:215], v[78:81]
	v_mfma_f32_16x16x32_f16 v[78:81], v[182:185], v[160:163], v[118:121]
	v_mfma_f32_16x16x32_f16 v[220:223], v[186:189], v[216:219], v[78:81]
	v_mfma_f32_16x16x32_f16 v[78:81], v[190:193], v[130:133], v[122:125]
	v_mfma_f32_16x16x32_f16 v[98:101], v[168:171], v[212:215], v[98:101]
	v_mfma_f32_16x16x32_f16 v[212:215], v[196:199], v[212:215], v[78:81]
	v_mfma_f32_16x16x32_f16 v[78:81], v[190:193], v[160:163], v[126:129]
	v_mfma_f32_16x16x32_f16 v[196:199], v[196:199], v[216:219], v[78:81]
	s_barrier
	ds_read_b128 v[110:113], v148
	ds_read_b128 v[130:133], v149
	ds_read_b128 v[216:219], v150
	ds_read_b128 v[224:227], v151
	s_nop 0
	ds_read_b128 v[78:81], v173 offset:32768
	ds_read_b128 v[114:117], v173 offset:33792
	ds_read_b128 v[118:121], v173 offset:34816
	ds_read_b128 v[134:137], v173 offset:35840
	ds_read_b128 v[138:141], v173 offset:36864
	ds_read_b128 v[168:171], v173 offset:37888
	ds_read_b128 v[174:177], v173 offset:38912
	ds_read_b128 v[228:231], v173 offset:39936
	s_waitcnt vmcnt(2)
	s_barrier
	s_waitcnt lgkmcnt(0)
	v_mfma_f32_16x16x32_f16 v[2:5], v[78:81], v[110:113], v[2:5]
	v_mfma_f32_16x16x32_f16 v[190:193], v[114:117], v[130:133], v[2:5]
	v_mfma_f32_16x16x32_f16 v[2:5], v[78:81], v[216:219], v[6:9]
	v_mfma_f32_16x16x32_f16 v[158:161], v[114:117], v[224:227], v[2:5]
	v_mfma_f32_16x16x32_f16 v[2:5], v[118:121], v[110:113], v[10:13]
	v_mfma_f32_16x16x32_f16 v[186:189], v[134:137], v[130:133], v[2:5]
	v_mfma_f32_16x16x32_f16 v[2:5], v[118:121], v[216:219], v[18:21]
	v_mfma_f32_16x16x32_f16 v[154:157], v[134:137], v[224:227], v[2:5]
	v_mfma_f32_16x16x32_f16 v[2:5], v[138:141], v[110:113], v[30:33]
	v_mfma_f32_16x16x32_f16 v[182:185], v[168:171], v[130:133], v[2:5]
	v_mfma_f32_16x16x32_f16 v[2:5], v[138:141], v[216:219], v[42:45]
	v_mfma_f32_16x16x32_f16 v[150:153], v[168:171], v[224:227], v[2:5]
	v_mfma_f32_16x16x32_f16 v[2:5], v[174:177], v[110:113], v[54:57]
	v_mfma_f32_16x16x32_f16 v[178:181], v[228:231], v[130:133], v[2:5]
	v_mfma_f32_16x16x32_f16 v[2:5], v[174:177], v[216:219], v[66:69]
	v_mfma_f32_16x16x32_f16 v[146:149], v[228:231], v[224:227], v[2:5]
	s_barrier
	s_nop 4
	ds_read_b128 v[2:5], v142
	ds_read_b128 v[6:9], v143
	ds_read_b128 v[10:13], v144
	ds_read_b128 v[18:21], v145
	s_waitcnt vmcnt(0)
	s_barrier
	s_waitcnt lgkmcnt(0)
	v_mfma_f32_16x16x32_f16 v[14:17], v[78:81], v[2:5], v[14:17]
	v_mfma_f32_16x16x32_f16 v[126:129], v[114:117], v[6:9], v[14:17]
	v_mfma_f32_16x16x32_f16 v[14:17], v[78:81], v[10:13], v[22:25]
	v_mfma_f32_16x16x32_f16 v[78:81], v[114:117], v[18:21], v[14:17]
	v_mfma_f32_16x16x32_f16 v[14:17], v[118:121], v[2:5], v[34:37]
	v_mfma_f32_16x16x32_f16 v[122:125], v[134:137], v[6:9], v[14:17]
	v_mfma_f32_16x16x32_f16 v[14:17], v[118:121], v[10:13], v[46:49]
	v_mfma_f32_16x16x32_f16 v[66:69], v[134:137], v[18:21], v[14:17]
	v_mfma_f32_16x16x32_f16 v[14:17], v[138:141], v[2:5], v[58:61]
	v_mfma_f32_16x16x32_f16 v[118:121], v[168:171], v[6:9], v[14:17]
	v_mfma_f32_16x16x32_f16 v[14:17], v[138:141], v[10:13], v[70:73]
	v_mfma_f32_16x16x32_f16 v[54:57], v[168:171], v[18:21], v[14:17]
	v_mfma_f32_16x16x32_f16 v[14:17], v[174:177], v[2:5], v[164:167]
	v_mfma_f32_16x16x32_f16 v[114:117], v[228:231], v[6:9], v[14:17]
	v_mfma_f32_16x16x32_f16 v[14:17], v[174:177], v[10:13], v[86:89]
	v_mfma_f32_16x16x32_f16 v[42:45], v[228:231], v[18:21], v[14:17]
	s_barrier
	s_nop 4
	ds_read_b128 v[14:17], v173 offset:49152
	ds_read_b128 v[22:25], v173 offset:50176
	ds_read_b128 v[30:33], v173 offset:51200
	ds_read_b128 v[34:37], v173 offset:52224
	ds_read_b128 v[46:49], v173 offset:53248
	ds_read_b128 v[58:61], v173 offset:54272
	ds_read_b128 v[70:73], v173 offset:55296
	ds_read_b128 v[86:89], v173 offset:56320
	s_barrier
	s_waitcnt lgkmcnt(0)
	v_mfma_f32_16x16x32_f16 v[26:29], v[14:17], v[110:113], v[26:29]
	v_mfma_f32_16x16x32_f16 v[174:177], v[22:25], v[130:133], v[26:29]
	v_mfma_f32_16x16x32_f16 v[26:29], v[14:17], v[216:219], v[38:41]
	v_mfma_f32_16x16x32_f16 v[142:145], v[22:25], v[224:227], v[26:29]
	v_mfma_f32_16x16x32_f16 v[26:29], v[30:33], v[110:113], v[50:53]
	v_mfma_f32_16x16x32_f16 v[170:173], v[34:37], v[130:133], v[26:29]
	v_mfma_f32_16x16x32_f16 v[26:29], v[30:33], v[216:219], v[62:65]
	v_mfma_f32_16x16x32_f16 v[138:141], v[34:37], v[224:227], v[26:29]
	v_mfma_f32_16x16x32_f16 v[26:29], v[46:49], v[110:113], v[74:77]
	v_mfma_f32_16x16x32_f16 v[166:169], v[58:61], v[130:133], v[26:29]
	v_mfma_f32_16x16x32_f16 v[26:29], v[46:49], v[216:219], v[82:85]
	v_mfma_f32_16x16x32_f16 v[134:137], v[58:61], v[224:227], v[26:29]
	v_mfma_f32_16x16x32_f16 v[26:29], v[70:73], v[110:113], v[90:93]
	v_mfma_f32_16x16x32_f16 v[162:165], v[86:89], v[130:133], v[26:29]
	v_mfma_f32_16x16x32_f16 v[26:29], v[70:73], v[216:219], v[94:97]
	v_mfma_f32_16x16x32_f16 v[130:133], v[86:89], v[224:227], v[26:29]
	v_mfma_f32_16x16x32_f16 v[26:29], v[14:17], v[2:5], v[98:101]
	v_mfma_f32_16x16x32_f16 v[14:17], v[14:17], v[10:13], v[102:105]
	v_mfma_f32_16x16x32_f16 v[38:41], v[22:25], v[18:21], v[14:17]
	v_mfma_f32_16x16x32_f16 v[14:17], v[30:33], v[2:5], v[106:109]
	v_mfma_f32_16x16x32_f16 v[106:109], v[34:37], v[6:9], v[14:17]
	v_mfma_f32_16x16x32_f16 v[14:17], v[30:33], v[10:13], v[200:203]
	v_mfma_f32_16x16x32_f16 v[110:113], v[22:25], v[6:9], v[26:29]
	v_mfma_f32_16x16x32_f16 v[26:29], v[34:37], v[18:21], v[14:17]
	v_mfma_f32_16x16x32_f16 v[14:17], v[46:49], v[2:5], v[204:207]
	v_mfma_f32_16x16x32_f16 v[2:5], v[70:73], v[2:5], v[212:215]
	v_mfma_f32_16x16x32_f16 v[102:105], v[58:61], v[6:9], v[14:17]
	v_mfma_f32_16x16x32_f16 v[14:17], v[46:49], v[10:13], v[220:223]
	v_mfma_f32_16x16x32_f16 v[98:101], v[86:89], v[6:9], v[2:5]
	v_mfma_f32_16x16x32_f16 v[2:5], v[70:73], v[10:13], v[196:199]
	v_mfma_f32_16x16x32_f16 v[14:17], v[58:61], v[18:21], v[14:17]
	v_mfma_f32_16x16x32_f16 v[2:5], v[86:89], v[18:21], v[2:5]
	s_cmpk_gt_u32 s65, 0xff
	s_barrier
	s_cbranch_scc1 .LBB7_242
	s_barrier

.LBB8_41:
	ds_read_b128 v[182:185], v171
	ds_read_b128 v[186:189], v173
	ds_read_b128 v[190:193], v174
	ds_read_b128 v[194:197], v175
	v_add_u32_e32 v177, 0xc000, v148
	v_lshl_add_u64 v[246:247], v[134:135], 0, s[44:45]
	v_add_u32_e32 v176, s48, v170
	s_mov_b32 m0, s75
	v_lshl_add_u64 v[178:179], v[246:247], 0, s[28:29]
	global_load_lds_dwordx4 v[178:179], off
	ds_read_b128 v[198:201], v176
	ds_read_b128 v[202:205], v176 offset:1024
	ds_read_b128 v[206:209], v176 offset:2048
	ds_read_b128 v[210:213], v176 offset:3072
	ds_read_b128 v[214:217], v176 offset:4096
	ds_read_b128 v[218:221], v176 offset:5120
	ds_read_b128 v[222:225], v176 offset:6144
	ds_read_b128 v[226:229], v176 offset:7168
	v_add_u32_e32 v178, 0xe000, v148
	v_lshl_add_u64 v[248:249], v[136:137], 0, s[44:45]
	s_mov_b32 m0, s76
	v_lshl_add_u64 v[230:231], v[248:249], 0, s[28:29]
	global_load_lds_dwordx4 v[230:231], off
	s_waitcnt lgkmcnt(8)
	s_barrier
	s_waitcnt lgkmcnt(0)
	v_mfma_f32_16x16x32_f16 v[126:129], v[198:201], v[182:185], v[126:129]
	v_mfma_f32_16x16x32_f16 v[122:125], v[198:201], v[190:193], v[122:125]
	v_mfma_f32_16x16x32_f16 v[118:121], v[206:209], v[182:185], v[118:121]
	v_mfma_f32_16x16x32_f16 v[114:117], v[206:209], v[190:193], v[114:117]
	v_mfma_f32_16x16x32_f16 v[110:113], v[214:217], v[182:185], v[110:113]
	v_mfma_f32_16x16x32_f16 v[106:109], v[214:217], v[190:193], v[106:109]
	v_mfma_f32_16x16x32_f16 v[102:105], v[222:225], v[182:185], v[102:105]
	v_mfma_f32_16x16x32_f16 v[98:101], v[222:225], v[190:193], v[98:101]
	v_mfma_f32_16x16x32_f16 v[126:129], v[202:205], v[186:189], v[126:129]
	v_mfma_f32_16x16x32_f16 v[122:125], v[202:205], v[194:197], v[122:125]
	v_mfma_f32_16x16x32_f16 v[118:121], v[210:213], v[186:189], v[118:121]
	v_mfma_f32_16x16x32_f16 v[114:117], v[210:213], v[194:197], v[114:117]
	v_mfma_f32_16x16x32_f16 v[110:113], v[218:221], v[186:189], v[110:113]
	v_mfma_f32_16x16x32_f16 v[106:109], v[218:221], v[194:197], v[106:109]
	v_mfma_f32_16x16x32_f16 v[102:105], v[226:229], v[186:189], v[102:105]
	v_mfma_f32_16x16x32_f16 v[98:101], v[226:229], v[194:197], v[98:101]
	s_barrier
	v_lshl_add_u64 v[250:251], v[138:139], 0, s[44:45]
	s_mov_b32 m0, s77
	v_lshl_add_u64 v[252:253], v[250:251], 0, s[30:31]
	global_load_lds_dwordx4 v[252:253], off
	ds_read_b128 v[230:233], v162
	ds_read_b128 v[234:237], v163
	ds_read_b128 v[238:241], v164
	ds_read_b128 v[242:245], v165
	v_lshl_add_u64 v[252:253], v[140:141], 0, s[44:45]
	s_mov_b32 m0, s78
	v_lshl_add_u64 v[254:255], v[252:253], 0, s[30:31]
	global_load_lds_dwordx4 v[254:255], off
	s_barrier
	s_waitcnt lgkmcnt(0)
	v_mfma_f32_16x16x32_f16 v[94:97], v[198:201], v[230:233], v[94:97]
	v_mfma_f32_16x16x32_f16 v[90:93], v[198:201], v[238:241], v[90:93]
	v_mfma_f32_16x16x32_f16 v[86:89], v[206:209], v[230:233], v[86:89]
	v_mfma_f32_16x16x32_f16 v[82:85], v[206:209], v[238:241], v[82:85]
	v_mfma_f32_16x16x32_f16 v[78:81], v[214:217], v[230:233], v[78:81]
	v_mfma_f32_16x16x32_f16 v[74:77], v[214:217], v[238:241], v[74:77]
	v_mfma_f32_16x16x32_f16 v[70:73], v[222:225], v[230:233], v[70:73]
	v_mfma_f32_16x16x32_f16 v[66:69], v[222:225], v[238:241], v[66:69]
	v_mfma_f32_16x16x32_f16 v[94:97], v[202:205], v[234:237], v[94:97]
	v_mfma_f32_16x16x32_f16 v[90:93], v[202:205], v[242:245], v[90:93]
	v_mfma_f32_16x16x32_f16 v[86:89], v[210:213], v[234:237], v[86:89]
	v_mfma_f32_16x16x32_f16 v[82:85], v[210:213], v[242:245], v[82:85]
	v_mfma_f32_16x16x32_f16 v[78:81], v[218:221], v[234:237], v[78:81]
	v_mfma_f32_16x16x32_f16 v[74:77], v[218:221], v[242:245], v[74:77]
	v_mfma_f32_16x16x32_f16 v[70:73], v[226:229], v[234:237], v[70:73]
	v_mfma_f32_16x16x32_f16 v[66:69], v[226:229], v[242:245], v[66:69]
	v_lshl_add_u64 v[254:255], v[246:247], 0, s[30:31]
	s_mov_b32 m0, s79
	s_barrier
	ds_read_b128 v[198:201], v176 offset:16384
	ds_read_b128 v[202:205], v176 offset:17408
	ds_read_b128 v[206:209], v176 offset:18432
	ds_read_b128 v[210:213], v176 offset:19456
	ds_read_b128 v[214:217], v176 offset:20480
	ds_read_b128 v[218:221], v176 offset:21504
	ds_read_b128 v[222:225], v176 offset:22528
	ds_read_b128 v[226:229], v176 offset:23552
	global_load_lds_dwordx4 v[254:255], off
	s_mov_b32 m0, s80
	v_lshl_add_u64 v[254:255], v[248:249], 0, s[30:31]
	global_load_lds_dwordx4 v[254:255], off
	s_barrier
	s_waitcnt lgkmcnt(0)
	v_mfma_f32_16x16x32_f16 v[62:65], v[198:201], v[182:185], v[62:65]
	v_mfma_f32_16x16x32_f16 v[58:61], v[198:201], v[190:193], v[58:61]
	v_mfma_f32_16x16x32_f16 v[54:57], v[206:209], v[182:185], v[54:57]
	v_mfma_f32_16x16x32_f16 v[50:53], v[206:209], v[190:193], v[50:53]
	v_mfma_f32_16x16x32_f16 v[46:49], v[214:217], v[182:185], v[46:49]
	v_mfma_f32_16x16x32_f16 v[42:45], v[214:217], v[190:193], v[42:45]
	v_mfma_f32_16x16x32_f16 v[38:41], v[222:225], v[182:185], v[38:41]
	v_mfma_f32_16x16x32_f16 v[34:37], v[222:225], v[190:193], v[34:37]
	v_mfma_f32_16x16x32_f16 v[62:65], v[202:205], v[186:189], v[62:65]
	v_mfma_f32_16x16x32_f16 v[58:61], v[202:205], v[194:197], v[58:61]
	v_mfma_f32_16x16x32_f16 v[54:57], v[210:213], v[186:189], v[54:57]
	v_mfma_f32_16x16x32_f16 v[50:53], v[210:213], v[194:197], v[50:53]
	v_mfma_f32_16x16x32_f16 v[46:49], v[218:221], v[186:189], v[46:49]
	v_mfma_f32_16x16x32_f16 v[42:45], v[218:221], v[194:197], v[42:45]
	v_mfma_f32_16x16x32_f16 v[38:41], v[226:229], v[186:189], v[38:41]
	v_mfma_f32_16x16x32_f16 v[34:37], v[226:229], v[194:197], v[34:37]
	s_barrier
	s_mov_b32 m0, s81
	v_lshl_add_u64 v[182:183], v[250:251], 0, s[34:35]
	global_load_lds_dwordx4 v[182:183], off
	s_mov_b32 m0, s82
	v_lshl_add_u64 v[182:183], v[252:253], 0, s[34:35]
	global_load_lds_dwordx4 v[182:183], off
	s_waitcnt vmcnt(6)
	s_barrier
	v_mfma_f32_16x16x32_f16 v[30:33], v[198:201], v[230:233], v[30:33]
	v_mfma_f32_16x16x32_f16 v[26:29], v[198:201], v[238:241], v[26:29]
	v_mfma_f32_16x16x32_f16 v[22:25], v[206:209], v[230:233], v[22:25]
	v_mfma_f32_16x16x32_f16 v[18:21], v[206:209], v[238:241], v[18:21]
	v_mfma_f32_16x16x32_f16 v[14:17], v[214:217], v[230:233], v[14:17]
	v_mfma_f32_16x16x32_f16 v[10:13], v[214:217], v[238:241], v[10:13]
	v_mfma_f32_16x16x32_f16 v[6:9], v[222:225], v[230:233], v[6:9]
	v_mfma_f32_16x16x32_f16 v[2:5], v[222:225], v[238:241], v[2:5]
	v_mfma_f32_16x16x32_f16 v[30:33], v[202:205], v[234:237], v[30:33]
	v_mfma_f32_16x16x32_f16 v[26:29], v[202:205], v[242:245], v[26:29]
	v_mfma_f32_16x16x32_f16 v[22:25], v[210:213], v[234:237], v[22:25]
	v_mfma_f32_16x16x32_f16 v[18:21], v[210:213], v[242:245], v[18:21]
	v_mfma_f32_16x16x32_f16 v[14:17], v[218:221], v[234:237], v[14:17]
	v_mfma_f32_16x16x32_f16 v[10:13], v[218:221], v[242:245], v[10:13]
	v_mfma_f32_16x16x32_f16 v[6:9], v[226:229], v[234:237], v[6:9]
	v_mfma_f32_16x16x32_f16 v[2:5], v[226:229], v[242:245], v[2:5]
	s_barrier
	ds_read_b128 v[182:185], v144
	ds_read_b128 v[186:189], v145
	ds_read_b128 v[190:193], v146
	ds_read_b128 v[194:197], v147
	s_mov_b32 m0, s83
	v_lshl_add_u64 v[230:231], v[246:247], 0, s[34:35]
	global_load_lds_dwordx4 v[230:231], off
	ds_read_b128 v[198:201], v176 offset:32768
	ds_read_b128 v[202:205], v176 offset:33792
	ds_read_b128 v[206:209], v176 offset:34816
	ds_read_b128 v[210:213], v176 offset:35840
	ds_read_b128 v[214:217], v176 offset:36864
	ds_read_b128 v[218:221], v176 offset:37888
	ds_read_b128 v[222:225], v176 offset:38912
	ds_read_b128 v[226:229], v176 offset:39936
	s_mov_b32 m0, s84
	v_lshl_add_u64 v[230:231], v[248:249], 0, s[34:35]
	global_load_lds_dwordx4 v[230:231], off
	s_waitcnt lgkmcnt(8)
	s_barrier
	s_waitcnt lgkmcnt(0)
	v_mfma_f32_16x16x32_f16 v[126:129], v[198:201], v[182:185], v[126:129]
	v_mfma_f32_16x16x32_f16 v[122:125], v[198:201], v[190:193], v[122:125]
	v_mfma_f32_16x16x32_f16 v[118:121], v[206:209], v[182:185], v[118:121]
	v_mfma_f32_16x16x32_f16 v[114:117], v[206:209], v[190:193], v[114:117]
	v_mfma_f32_16x16x32_f16 v[110:113], v[214:217], v[182:185], v[110:113]
	v_mfma_f32_16x16x32_f16 v[106:109], v[214:217], v[190:193], v[106:109]
	v_mfma_f32_16x16x32_f16 v[102:105], v[222:225], v[182:185], v[102:105]
	v_mfma_f32_16x16x32_f16 v[98:101], v[222:225], v[190:193], v[98:101]
	v_mfma_f32_16x16x32_f16 v[126:129], v[202:205], v[186:189], v[126:129]
	v_mfma_f32_16x16x32_f16 v[122:125], v[202:205], v[194:197], v[122:125]
	v_mfma_f32_16x16x32_f16 v[118:121], v[210:213], v[186:189], v[118:121]
	v_mfma_f32_16x16x32_f16 v[114:117], v[210:213], v[194:197], v[114:117]
	v_mfma_f32_16x16x32_f16 v[110:113], v[218:221], v[186:189], v[110:113]
	v_mfma_f32_16x16x32_f16 v[106:109], v[218:221], v[194:197], v[106:109]
	v_mfma_f32_16x16x32_f16 v[102:105], v[226:229], v[186:189], v[102:105]
	v_mfma_f32_16x16x32_f16 v[98:101], v[226:229], v[194:197], v[98:101]
	s_barrier
	s_mov_b32 m0, s85
	v_lshl_add_u64 v[254:255], v[250:251], 0, s[36:37]
	global_load_lds_dwordx4 v[254:255], off
	ds_read_b128 v[230:233], v150
	ds_read_b128 v[234:237], v151
	ds_read_b128 v[238:241], v152
	ds_read_b128 v[242:245], v153
	s_mov_b32 m0, s86
	v_lshl_add_u64 v[254:255], v[252:253], 0, s[36:37]
	global_load_lds_dwordx4 v[254:255], off
	s_barrier
	s_waitcnt lgkmcnt(0)
	v_mfma_f32_16x16x32_f16 v[94:97], v[198:201], v[230:233], v[94:97]
	v_mfma_f32_16x16x32_f16 v[90:93], v[198:201], v[238:241], v[90:93]
	v_mfma_f32_16x16x32_f16 v[86:89], v[206:209], v[230:233], v[86:89]
	v_mfma_f32_16x16x32_f16 v[82:85], v[206:209], v[238:241], v[82:85]
	v_mfma_f32_16x16x32_f16 v[78:81], v[214:217], v[230:233], v[78:81]
	v_mfma_f32_16x16x32_f16 v[74:77], v[214:217], v[238:241], v[74:77]
	v_mfma_f32_16x16x32_f16 v[70:73], v[222:225], v[230:233], v[70:73]
	v_mfma_f32_16x16x32_f16 v[66:69], v[222:225], v[238:241], v[66:69]
	v_mfma_f32_16x16x32_f16 v[94:97], v[202:205], v[234:237], v[94:97]
	v_mfma_f32_16x16x32_f16 v[90:93], v[202:205], v[242:245], v[90:93]
	v_mfma_f32_16x16x32_f16 v[86:89], v[210:213], v[234:237], v[86:89]
	v_mfma_f32_16x16x32_f16 v[82:85], v[210:213], v[242:245], v[82:85]
	v_mfma_f32_16x16x32_f16 v[78:81], v[218:221], v[234:237], v[78:81]
	v_mfma_f32_16x16x32_f16 v[74:77], v[218:221], v[242:245], v[74:77]
	v_mfma_f32_16x16x32_f16 v[70:73], v[226:229], v[234:237], v[70:73]
	v_mfma_f32_16x16x32_f16 v[66:69], v[226:229], v[242:245], v[66:69]
	v_lshl_add_u64 v[246:247], v[246:247], 0, s[36:37]
	s_mov_b32 m0, s87
	s_barrier
	ds_read_b128 v[198:201], v176 offset:49152
	ds_read_b128 v[202:205], v176 offset:50176
	ds_read_b128 v[206:209], v176 offset:51200
	ds_read_b128 v[210:213], v176 offset:52224
	ds_read_b128 v[214:217], v176 offset:53248
	ds_read_b128 v[218:221], v176 offset:54272
	ds_read_b128 v[222:225], v176 offset:55296
	ds_read_b128 v[226:229], v176 offset:56320
	global_load_lds_dwordx4 v[246:247], off
	s_mov_b32 m0, s88
	v_lshl_add_u64 v[246:247], v[248:249], 0, s[36:37]
	global_load_lds_dwordx4 v[246:247], off
	s_barrier
	s_waitcnt lgkmcnt(0)
	v_mfma_f32_16x16x32_f16 v[62:65], v[198:201], v[182:185], v[62:65]
	v_mfma_f32_16x16x32_f16 v[58:61], v[198:201], v[190:193], v[58:61]
	v_mfma_f32_16x16x32_f16 v[54:57], v[206:209], v[182:185], v[54:57]
	v_mfma_f32_16x16x32_f16 v[50:53], v[206:209], v[190:193], v[50:53]
	v_mfma_f32_16x16x32_f16 v[46:49], v[214:217], v[182:185], v[46:49]
	v_mfma_f32_16x16x32_f16 v[42:45], v[214:217], v[190:193], v[42:45]
	v_mfma_f32_16x16x32_f16 v[38:41], v[222:225], v[182:185], v[38:41]
	v_mfma_f32_16x16x32_f16 v[34:37], v[222:225], v[190:193], v[34:37]
	v_mfma_f32_16x16x32_f16 v[62:65], v[202:205], v[186:189], v[62:65]
	v_mfma_f32_16x16x32_f16 v[58:61], v[202:205], v[194:197], v[58:61]
	v_mfma_f32_16x16x32_f16 v[54:57], v[210:213], v[186:189], v[54:57]
	v_mfma_f32_16x16x32_f16 v[50:53], v[210:213], v[194:197], v[50:53]
	v_mfma_f32_16x16x32_f16 v[46:49], v[218:221], v[186:189], v[46:49]
	v_mfma_f32_16x16x32_f16 v[42:45], v[218:221], v[194:197], v[42:45]
	v_mfma_f32_16x16x32_f16 v[38:41], v[226:229], v[186:189], v[38:41]
	v_mfma_f32_16x16x32_f16 v[34:37], v[226:229], v[194:197], v[34:37]
	s_barrier
	s_mov_b32 m0, s89
	v_lshl_add_u64 v[182:183], v[250:251], 0, s[38:39]
	global_load_lds_dwordx4 v[182:183], off
	s_mov_b32 m0, s90
	v_lshl_add_u64 v[182:183], v[252:253], 0, s[38:39]
	global_load_lds_dwordx4 v[182:183], off
	s_waitcnt vmcnt(6)
	s_barrier
	v_mfma_f32_16x16x32_f16 v[30:33], v[198:201], v[230:233], v[30:33]
	v_mfma_f32_16x16x32_f16 v[26:29], v[198:201], v[238:241], v[26:29]
	v_mfma_f32_16x16x32_f16 v[22:25], v[206:209], v[230:233], v[22:25]
	v_mfma_f32_16x16x32_f16 v[18:21], v[206:209], v[238:241], v[18:21]
	v_mfma_f32_16x16x32_f16 v[14:17], v[214:217], v[230:233], v[14:17]
	v_mfma_f32_16x16x32_f16 v[10:13], v[214:217], v[238:241], v[10:13]
	v_mfma_f32_16x16x32_f16 v[6:9], v[222:225], v[230:233], v[6:9]
	v_mfma_f32_16x16x32_f16 v[2:5], v[222:225], v[238:241], v[2:5]
	v_mfma_f32_16x16x32_f16 v[30:33], v[202:205], v[234:237], v[30:33]
	v_mfma_f32_16x16x32_f16 v[26:29], v[202:205], v[242:245], v[26:29]
	v_mfma_f32_16x16x32_f16 v[22:25], v[210:213], v[234:237], v[22:25]
	v_mfma_f32_16x16x32_f16 v[18:21], v[210:213], v[242:245], v[18:21]
	v_mfma_f32_16x16x32_f16 v[14:17], v[218:221], v[234:237], v[14:17]
	v_mfma_f32_16x16x32_f16 v[10:13], v[218:221], v[242:245], v[10:13]
	v_mfma_f32_16x16x32_f16 v[6:9], v[226:229], v[234:237], v[6:9]
	v_mfma_f32_16x16x32_f16 v[2:5], v[226:229], v[242:245], v[2:5]
	s_add_i32 s46, s46, 2
	s_add_u32 s44, s44, 0x100
	s_addc_u32 s45, s45, 0
	s_cmp_lt_u32 s46, 4
	s_barrier
	s_cbranch_scc1 .LBB8_41
	s_add_u32 s42, s42, 0x20380
	s_addc_u32 s43, s43, 0
	v_readfirstlane_b32 s44, v177
	v_lshl_add_u64 v[130:131], v[130:131], 1, s[42:43]
	s_mov_b32 m0, s44
	ds_read_b128 v[134:137], v171
	ds_read_b128 v[138:141], v173
	ds_read_b128 v[154:157], v174
	ds_read_b128 v[168:171], v175
	ds_read_b128 v[182:185], v176
	ds_read_b128 v[186:189], v176 offset:1024
	ds_read_b128 v[190:193], v176 offset:2048
	ds_read_b128 v[194:197], v176 offset:3072
	ds_read_b128 v[198:201], v176 offset:4096
	ds_read_b128 v[202:205], v176 offset:5120
	ds_read_b128 v[206:209], v176 offset:6144
	ds_read_b128 v[210:213], v176 offset:7168
	global_load_lds_dwordx4 v[130:131], off
	v_lshl_add_u64 v[130:131], v[132:133], 1, s[42:43]
	v_readfirstlane_b32 s42, v178
	s_mov_b32 m0, s42
	s_nop 0
	global_load_lds_dwordx4 v[130:131], off
	s_barrier
	s_waitcnt lgkmcnt(0)
	v_mfma_f32_16x16x32_f16 v[122:125], v[182:185], v[154:157], v[122:125]
	v_mfma_f32_16x16x32_f16 v[110:113], v[198:201], v[134:137], v[110:113]
	v_mfma_f32_16x16x32_f16 v[98:101], v[206:209], v[154:157], v[98:101]
	v_mfma_f32_16x16x32_f16 v[126:129], v[182:185], v[134:137], v[126:129]
	v_mfma_f32_16x16x32_f16 v[122:125], v[186:189], v[168:171], v[122:125]
	v_mfma_f32_16x16x32_f16 v[118:121], v[190:193], v[134:137], v[118:121]
	v_mfma_f32_16x16x32_f16 v[114:117], v[190:193], v[154:157], v[114:117]
	v_mfma_f32_16x16x32_f16 v[130:133], v[202:205], v[138:141], v[110:113]
	v_mfma_f32_16x16x32_f16 v[106:109], v[198:201], v[154:157], v[106:109]
	v_mfma_f32_16x16x32_f16 v[102:105], v[206:209], v[134:137], v[102:105]
	v_mfma_f32_16x16x32_f16 v[98:101], v[210:213], v[168:171], v[98:101]
	v_mfma_f32_16x16x32_f16 v[126:129], v[186:189], v[138:141], v[126:129]
	v_mfma_f32_16x16x32_f16 v[118:121], v[194:197], v[138:141], v[118:121]
	v_mfma_f32_16x16x32_f16 v[114:117], v[194:197], v[168:171], v[114:117]
	v_mfma_f32_16x16x32_f16 v[214:217], v[202:205], v[168:171], v[106:109]
	v_mfma_f32_16x16x32_f16 v[102:105], v[210:213], v[138:141], v[102:105]
	s_barrier
	ds_read_b128 v[106:109], v162
	ds_read_b128 v[110:113], v163
	ds_read_b128 v[160:163], v164
	ds_read_b128 v[218:221], v165
	s_barrier
	s_waitcnt lgkmcnt(0)
	v_mfma_f32_16x16x32_f16 v[82:85], v[190:193], v[160:163], v[82:85]
	v_mfma_f32_16x16x32_f16 v[78:81], v[198:201], v[106:109], v[78:81]
	v_mfma_f32_16x16x32_f16 v[74:77], v[198:201], v[160:163], v[74:77]
	v_mfma_f32_16x16x32_f16 v[70:73], v[206:209], v[106:109], v[70:73]
	v_mfma_f32_16x16x32_f16 v[66:69], v[206:209], v[160:163], v[66:69]
	v_mfma_f32_16x16x32_f16 v[94:97], v[182:185], v[106:109], v[94:97]
	v_mfma_f32_16x16x32_f16 v[90:93], v[182:185], v[160:163], v[90:93]
	v_mfma_f32_16x16x32_f16 v[86:89], v[190:193], v[106:109], v[86:89]
	v_mfma_f32_16x16x32_f16 v[82:85], v[194:197], v[218:221], v[82:85]
	v_mfma_f32_16x16x32_f16 v[78:81], v[202:205], v[110:113], v[78:81]
	v_mfma_f32_16x16x32_f16 v[74:77], v[202:205], v[218:221], v[74:77]
	v_mfma_f32_16x16x32_f16 v[70:73], v[210:213], v[110:113], v[70:73]
	v_mfma_f32_16x16x32_f16 v[66:69], v[210:213], v[218:221], v[66:69]
	v_mfma_f32_16x16x32_f16 v[222:225], v[186:189], v[110:113], v[94:97]
	v_mfma_f32_16x16x32_f16 v[182:185], v[186:189], v[218:221], v[90:93]
	v_mfma_f32_16x16x32_f16 v[86:89], v[194:197], v[110:113], v[86:89]
	s_barrier
	ds_read_b128 v[90:93], v176 offset:16384
	ds_read_b128 v[94:97], v176 offset:17408
	ds_read_b128 v[186:189], v176 offset:18432
	ds_read_b128 v[190:193], v176 offset:19456
	ds_read_b128 v[194:197], v176 offset:20480
	ds_read_b128 v[198:201], v176 offset:21504
	ds_read_b128 v[202:205], v176 offset:22528
	ds_read_b128 v[206:209], v176 offset:23552
	s_waitcnt vmcnt(4)
	s_barrier
	s_waitcnt lgkmcnt(0)
	v_mfma_f32_16x16x32_f16 v[46:49], v[194:197], v[134:137], v[46:49]
	v_mfma_f32_16x16x32_f16 v[42:45], v[194:197], v[154:157], v[42:45]
	v_mfma_f32_16x16x32_f16 v[38:41], v[202:205], v[134:137], v[38:41]
	v_mfma_f32_16x16x32_f16 v[34:37], v[202:205], v[154:157], v[34:37]
	v_mfma_f32_16x16x32_f16 v[62:65], v[90:93], v[134:137], v[62:65]
	v_mfma_f32_16x16x32_f16 v[58:61], v[90:93], v[154:157], v[58:61]
	v_mfma_f32_16x16x32_f16 v[54:57], v[186:189], v[134:137], v[54:57]
	v_mfma_f32_16x16x32_f16 v[50:53], v[186:189], v[154:157], v[50:53]
	v_mfma_f32_16x16x32_f16 v[46:49], v[198:201], v[138:141], v[46:49]
	v_mfma_f32_16x16x32_f16 v[42:45], v[198:201], v[168:171], v[42:45]
	v_mfma_f32_16x16x32_f16 v[38:41], v[206:209], v[138:141], v[38:41]
	v_mfma_f32_16x16x32_f16 v[34:37], v[206:209], v[168:171], v[34:37]
	v_mfma_f32_16x16x32_f16 v[210:213], v[94:97], v[138:141], v[62:65]
	v_mfma_f32_16x16x32_f16 v[226:229], v[94:97], v[168:171], v[58:61]
	v_mfma_f32_16x16x32_f16 v[230:233], v[190:193], v[138:141], v[54:57]
	v_mfma_f32_16x16x32_f16 v[234:237], v[190:193], v[168:171], v[50:53]
	v_mfma_f32_16x16x32_f16 v[2:5], v[202:205], v[160:163], v[2:5]
	v_mfma_f32_16x16x32_f16 v[30:33], v[90:93], v[106:109], v[30:33]
	v_mfma_f32_16x16x32_f16 v[26:29], v[90:93], v[160:163], v[26:29]
	v_mfma_f32_16x16x32_f16 v[22:25], v[186:189], v[106:109], v[22:25]
	v_mfma_f32_16x16x32_f16 v[18:21], v[186:189], v[160:163], v[18:21]
	v_mfma_f32_16x16x32_f16 v[14:17], v[194:197], v[106:109], v[14:17]
	v_mfma_f32_16x16x32_f16 v[10:13], v[194:197], v[160:163], v[10:13]
	v_mfma_f32_16x16x32_f16 v[6:9], v[202:205], v[106:109], v[6:9]
	v_mfma_f32_16x16x32_f16 v[2:5], v[206:209], v[218:221], v[2:5]
	v_mfma_f32_16x16x32_f16 v[138:141], v[94:97], v[110:113], v[30:33]
	v_mfma_f32_16x16x32_f16 v[168:171], v[94:97], v[218:221], v[26:29]
	v_mfma_f32_16x16x32_f16 v[238:241], v[190:193], v[110:113], v[22:25]
	v_mfma_f32_16x16x32_f16 v[186:189], v[190:193], v[218:221], v[18:21]
	v_mfma_f32_16x16x32_f16 v[190:193], v[198:201], v[110:113], v[14:17]
	v_mfma_f32_16x16x32_f16 v[194:197], v[198:201], v[218:221], v[10:13]
	v_mfma_f32_16x16x32_f16 v[198:201], v[206:209], v[110:113], v[6:9]
	s_barrier
	s_nop 0
	ds_read_b128 v[6:9], v144
	ds_read_b128 v[10:13], v145
	ds_read_b128 v[14:17], v146
	ds_read_b128 v[160:163], v147
	ds_read_b128 v[18:21], v176 offset:32768
	ds_read_b128 v[22:25], v176 offset:33792
	ds_read_b128 v[26:29], v176 offset:34816
	ds_read_b128 v[50:53], v176 offset:35840
	ds_read_b128 v[202:205], v176 offset:36864
	ds_read_b128 v[206:209], v176 offset:37888
	ds_read_b128 v[218:221], v176 offset:38912
	ds_read_b128 v[242:245], v176 offset:39936
	s_waitcnt vmcnt(2)
	s_barrier
	s_waitcnt lgkmcnt(0)
	v_mfma_f32_16x16x32_f16 v[30:33], v[18:21], v[6:9], v[126:129]
	v_mfma_f32_16x16x32_f16 v[154:157], v[22:25], v[10:13], v[30:33]
	v_mfma_f32_16x16x32_f16 v[30:33], v[18:21], v[14:17], v[122:125]
	v_mfma_f32_16x16x32_f16 v[110:113], v[22:25], v[160:163], v[30:33]
	v_mfma_f32_16x16x32_f16 v[30:33], v[26:29], v[6:9], v[118:121]
	v_mfma_f32_16x16x32_f16 v[146:149], v[50:53], v[10:13], v[30:33]
	v_mfma_f32_16x16x32_f16 v[30:33], v[26:29], v[14:17], v[114:117]
	v_mfma_f32_16x16x32_f16 v[106:109], v[50:53], v[160:163], v[30:33]
	v_mfma_f32_16x16x32_f16 v[30:33], v[202:205], v[6:9], v[130:133]
	v_mfma_f32_16x16x32_f16 v[142:145], v[206:209], v[10:13], v[30:33]
	v_mfma_f32_16x16x32_f16 v[30:33], v[202:205], v[14:17], v[214:217]
	v_mfma_f32_16x16x32_f16 v[94:97], v[206:209], v[160:163], v[30:33]
	v_mfma_f32_16x16x32_f16 v[30:33], v[218:221], v[6:9], v[102:105]
	v_mfma_f32_16x16x32_f16 v[134:137], v[242:245], v[10:13], v[30:33]
	v_mfma_f32_16x16x32_f16 v[30:33], v[218:221], v[14:17], v[98:101]
	v_mfma_f32_16x16x32_f16 v[90:93], v[242:245], v[160:163], v[30:33]
	s_barrier
	ds_read_b128 v[102:105], v150
	ds_read_b128 v[114:117], v151
	ds_read_b128 v[118:121], v152
	ds_read_b128 v[126:129], v153
	s_waitcnt vmcnt(0)
	s_barrier
	s_waitcnt lgkmcnt(0)
	v_mfma_f32_16x16x32_f16 v[30:33], v[18:21], v[102:105], v[222:225]
	v_mfma_f32_16x16x32_f16 v[18:21], v[18:21], v[118:121], v[182:185]
	v_mfma_f32_16x16x32_f16 v[62:65], v[22:25], v[114:117], v[30:33]
	v_mfma_f32_16x16x32_f16 v[30:33], v[22:25], v[126:129], v[18:21]
	v_mfma_f32_16x16x32_f16 v[18:21], v[26:29], v[102:105], v[86:89]
	v_mfma_f32_16x16x32_f16 v[58:61], v[50:53], v[114:117], v[18:21]
	v_mfma_f32_16x16x32_f16 v[18:21], v[26:29], v[118:121], v[82:85]
	v_mfma_f32_16x16x32_f16 v[26:29], v[50:53], v[126:129], v[18:21]
	v_mfma_f32_16x16x32_f16 v[18:21], v[202:205], v[102:105], v[78:81]
	v_mfma_f32_16x16x32_f16 v[54:57], v[206:209], v[114:117], v[18:21]
	v_mfma_f32_16x16x32_f16 v[18:21], v[202:205], v[118:121], v[74:77]
	v_mfma_f32_16x16x32_f16 v[22:25], v[206:209], v[126:129], v[18:21]
	v_mfma_f32_16x16x32_f16 v[18:21], v[218:221], v[102:105], v[70:73]
	v_mfma_f32_16x16x32_f16 v[50:53], v[242:245], v[114:117], v[18:21]
	v_mfma_f32_16x16x32_f16 v[18:21], v[218:221], v[118:121], v[66:69]
	v_mfma_f32_16x16x32_f16 v[18:21], v[242:245], v[126:129], v[18:21]
	s_barrier
	ds_read_b128 v[86:89], v176 offset:49152
	ds_read_b128 v[150:153], v176 offset:50176
	ds_read_b128 v[182:185], v176 offset:51200
	ds_read_b128 v[202:205], v176 offset:52224
	ds_read_b128 v[206:209], v176 offset:53248
	ds_read_b128 v[214:217], v176 offset:54272
	ds_read_b128 v[218:221], v176 offset:55296
	ds_read_b128 v[174:177], v176 offset:56320
	s_barrier
	s_waitcnt lgkmcnt(0)
	v_mfma_f32_16x16x32_f16 v[66:69], v[86:89], v[6:9], v[210:213]
	v_mfma_f32_16x16x32_f16 v[130:133], v[150:153], v[10:13], v[66:69]
	v_mfma_f32_16x16x32_f16 v[66:69], v[86:89], v[14:17], v[226:229]
	v_mfma_f32_16x16x32_f16 v[78:81], v[150:153], v[160:163], v[66:69]
	v_mfma_f32_16x16x32_f16 v[66:69], v[182:185], v[6:9], v[230:233]
	v_mfma_f32_16x16x32_f16 v[46:49], v[206:209], v[6:9], v[46:49]
	v_mfma_f32_16x16x32_f16 v[6:9], v[218:221], v[6:9], v[38:41]
	v_mfma_f32_16x16x32_f16 v[122:125], v[202:205], v[10:13], v[66:69]
	v_mfma_f32_16x16x32_f16 v[66:69], v[182:185], v[14:17], v[234:237]
	v_mfma_f32_16x16x32_f16 v[42:45], v[206:209], v[14:17], v[42:45]
	v_mfma_f32_16x16x32_f16 v[82:85], v[174:177], v[10:13], v[6:9]
	v_mfma_f32_16x16x32_f16 v[6:9], v[218:221], v[14:17], v[34:37]
	v_mfma_f32_16x16x32_f16 v[74:77], v[202:205], v[160:163], v[66:69]
	v_mfma_f32_16x16x32_f16 v[98:101], v[214:217], v[10:13], v[46:49]
	v_mfma_f32_16x16x32_f16 v[70:73], v[214:217], v[160:163], v[42:45]
	v_mfma_f32_16x16x32_f16 v[66:69], v[174:177], v[160:163], v[6:9]
	v_mfma_f32_16x16x32_f16 v[6:9], v[86:89], v[102:105], v[138:141]
	v_mfma_f32_16x16x32_f16 v[46:49], v[150:153], v[114:117], v[6:9]
	v_mfma_f32_16x16x32_f16 v[6:9], v[86:89], v[118:121], v[168:171]
	v_mfma_f32_16x16x32_f16 v[14:17], v[150:153], v[126:129], v[6:9]
	v_mfma_f32_16x16x32_f16 v[6:9], v[182:185], v[102:105], v[238:241]
	v_mfma_f32_16x16x32_f16 v[42:45], v[202:205], v[114:117], v[6:9]
	v_mfma_f32_16x16x32_f16 v[6:9], v[182:185], v[118:121], v[186:189]
	v_mfma_f32_16x16x32_f16 v[10:13], v[202:205], v[126:129], v[6:9]
	v_mfma_f32_16x16x32_f16 v[6:9], v[206:209], v[102:105], v[190:193]
	v_mfma_f32_16x16x32_f16 v[38:41], v[214:217], v[114:117], v[6:9]
	v_mfma_f32_16x16x32_f16 v[6:9], v[206:209], v[118:121], v[194:197]
	v_mfma_f32_16x16x32_f16 v[34:37], v[218:221], v[102:105], v[198:201]
	v_mfma_f32_16x16x32_f16 v[2:5], v[218:221], v[118:121], v[2:5]
	v_mfma_f32_16x16x32_f16 v[6:9], v[214:217], v[126:129], v[6:9]
	v_mfma_f32_16x16x32_f16 v[34:37], v[174:177], v[114:117], v[34:37]
	v_mfma_f32_16x16x32_f16 v[2:5], v[174:177], v[126:129], v[2:5]
	s_cmpk_gt_u32 s62, 0xff
	s_barrier
	s_cbranch_scc1 .LBB8_44
	s_barrier

.LBB9_38:
	ds_read_b128 v[176:179], v169
	ds_read_b128 v[180:183], v170
	ds_read_b128 v[184:187], v171
	ds_read_b128 v[188:191], v172
	v_add_u32_e32 v174, 0xc000, v152
	v_lshl_add_u64 v[192:193], v[136:137], 0, s[42:43]
	v_add_u32_e32 v175, 0xe000, v152
	v_add_u32_e32 v173, s39, v168
	v_lshl_add_u64 v[230:231], v[192:193], 0, s[10:11]
	s_mov_b32 m0, s65
	v_lshl_add_u64 v[246:247], v[134:135], 0, s[42:43]
	ds_read_b128 v[198:201], v173
	ds_read_b128 v[202:205], v173 offset:1024
	ds_read_b128 v[206:209], v173 offset:2048
	ds_read_b128 v[210:213], v173 offset:3072
	ds_read_b128 v[214:217], v173 offset:4096
	ds_read_b128 v[218:221], v173 offset:5120
	ds_read_b128 v[222:225], v173 offset:6144
	ds_read_b128 v[226:229], v173 offset:7168
	global_load_lds_dwordx4 v[230:231], off
	s_mov_b32 m0, s66
	v_lshl_add_u64 v[230:231], v[246:247], 0, s[10:11]
	global_load_lds_dwordx4 v[230:231], off
	s_waitcnt lgkmcnt(8)
	s_barrier
	s_waitcnt lgkmcnt(0)
	v_mfma_f32_16x16x32_f16 v[2:5], v[198:201], v[176:179], v[2:5]
	v_mfma_f32_16x16x32_f16 v[6:9], v[198:201], v[184:187], v[6:9]
	v_mfma_f32_16x16x32_f16 v[10:13], v[206:209], v[176:179], v[10:13]
	v_mfma_f32_16x16x32_f16 v[18:21], v[206:209], v[184:187], v[18:21]
	v_mfma_f32_16x16x32_f16 v[30:33], v[214:217], v[176:179], v[30:33]
	v_mfma_f32_16x16x32_f16 v[42:45], v[214:217], v[184:187], v[42:45]
	v_mfma_f32_16x16x32_f16 v[54:57], v[222:225], v[176:179], v[54:57]
	v_mfma_f32_16x16x32_f16 v[66:69], v[222:225], v[184:187], v[66:69]
	v_mfma_f32_16x16x32_f16 v[2:5], v[202:205], v[180:183], v[2:5]
	v_mfma_f32_16x16x32_f16 v[6:9], v[202:205], v[188:191], v[6:9]
	v_mfma_f32_16x16x32_f16 v[10:13], v[210:213], v[180:183], v[10:13]
	v_mfma_f32_16x16x32_f16 v[18:21], v[210:213], v[188:191], v[18:21]
	v_mfma_f32_16x16x32_f16 v[30:33], v[218:221], v[180:183], v[30:33]
	v_mfma_f32_16x16x32_f16 v[42:45], v[218:221], v[188:191], v[42:45]
	v_mfma_f32_16x16x32_f16 v[54:57], v[226:229], v[180:183], v[54:57]
	v_mfma_f32_16x16x32_f16 v[66:69], v[226:229], v[188:191], v[66:69]
	s_barrier
	v_lshl_add_u64 v[248:249], v[140:141], 0, s[42:43]
	s_mov_b32 m0, s67
	v_lshl_add_u64 v[250:251], v[248:249], 0, s[26:27]
	global_load_lds_dwordx4 v[250:251], off
	ds_read_b128 v[230:233], v161
	ds_read_b128 v[234:237], v162
	ds_read_b128 v[238:241], v163
	ds_read_b128 v[242:245], v164
	v_lshl_add_u64 v[250:251], v[138:139], 0, s[42:43]
	s_mov_b32 m0, s68
	v_lshl_add_u64 v[252:253], v[250:251], 0, s[26:27]
	global_load_lds_dwordx4 v[252:253], off
	s_barrier
	s_waitcnt lgkmcnt(0)
	v_mfma_f32_16x16x32_f16 v[14:17], v[198:201], v[230:233], v[14:17]
	v_mfma_f32_16x16x32_f16 v[22:25], v[198:201], v[238:241], v[22:25]
	v_mfma_f32_16x16x32_f16 v[34:37], v[206:209], v[230:233], v[34:37]
	v_mfma_f32_16x16x32_f16 v[46:49], v[206:209], v[238:241], v[46:49]
	v_mfma_f32_16x16x32_f16 v[58:61], v[214:217], v[230:233], v[58:61]
	v_mfma_f32_16x16x32_f16 v[70:73], v[214:217], v[238:241], v[70:73]
	v_mfma_f32_16x16x32_f16 v[78:81], v[222:225], v[230:233], v[78:81]
	v_mfma_f32_16x16x32_f16 v[86:89], v[222:225], v[238:241], v[86:89]
	v_mfma_f32_16x16x32_f16 v[14:17], v[202:205], v[234:237], v[14:17]
	v_mfma_f32_16x16x32_f16 v[22:25], v[202:205], v[242:245], v[22:25]
	v_mfma_f32_16x16x32_f16 v[34:37], v[210:213], v[234:237], v[34:37]
	v_mfma_f32_16x16x32_f16 v[46:49], v[210:213], v[242:245], v[46:49]
	v_mfma_f32_16x16x32_f16 v[58:61], v[218:221], v[234:237], v[58:61]
	v_mfma_f32_16x16x32_f16 v[70:73], v[218:221], v[242:245], v[70:73]
	v_mfma_f32_16x16x32_f16 v[78:81], v[226:229], v[234:237], v[78:81]
	v_mfma_f32_16x16x32_f16 v[86:89], v[226:229], v[242:245], v[86:89]
	v_lshl_add_u64 v[252:253], v[192:193], 0, s[26:27]
	s_mov_b32 m0, s69
	s_barrier
	ds_read_b128 v[198:201], v173 offset:16384
	ds_read_b128 v[202:205], v173 offset:17408
	ds_read_b128 v[206:209], v173 offset:18432
	ds_read_b128 v[210:213], v173 offset:19456
	ds_read_b128 v[214:217], v173 offset:20480
	ds_read_b128 v[218:221], v173 offset:21504
	ds_read_b128 v[222:225], v173 offset:22528
	ds_read_b128 v[226:229], v173 offset:23552
	global_load_lds_dwordx4 v[252:253], off
	s_mov_b32 m0, s70
	v_lshl_add_u64 v[252:253], v[246:247], 0, s[26:27]
	global_load_lds_dwordx4 v[252:253], off
	s_barrier
	s_waitcnt lgkmcnt(0)
	v_mfma_f32_16x16x32_f16 v[26:29], v[198:201], v[176:179], v[26:29]
	v_mfma_f32_16x16x32_f16 v[38:41], v[198:201], v[184:187], v[38:41]
	v_mfma_f32_16x16x32_f16 v[50:53], v[206:209], v[176:179], v[50:53]
	v_mfma_f32_16x16x32_f16 v[62:65], v[206:209], v[184:187], v[62:65]
	v_mfma_f32_16x16x32_f16 v[74:77], v[214:217], v[176:179], v[74:77]
	v_mfma_f32_16x16x32_f16 v[82:85], v[214:217], v[184:187], v[82:85]
	v_mfma_f32_16x16x32_f16 v[90:93], v[222:225], v[176:179], v[90:93]
	v_mfma_f32_16x16x32_f16 v[94:97], v[222:225], v[184:187], v[94:97]
	v_mfma_f32_16x16x32_f16 v[26:29], v[202:205], v[180:183], v[26:29]
	v_mfma_f32_16x16x32_f16 v[38:41], v[202:205], v[188:191], v[38:41]
	v_mfma_f32_16x16x32_f16 v[50:53], v[210:213], v[180:183], v[50:53]
	v_mfma_f32_16x16x32_f16 v[62:65], v[210:213], v[188:191], v[62:65]
	v_mfma_f32_16x16x32_f16 v[74:77], v[218:221], v[180:183], v[74:77]
	v_mfma_f32_16x16x32_f16 v[82:85], v[218:221], v[188:191], v[82:85]
	v_mfma_f32_16x16x32_f16 v[90:93], v[226:229], v[180:183], v[90:93]
	v_mfma_f32_16x16x32_f16 v[94:97], v[226:229], v[188:191], v[94:97]
	s_barrier
	s_mov_b32 m0, s71
	v_lshl_add_u64 v[176:177], v[248:249], 0, s[28:29]
	global_load_lds_dwordx4 v[176:177], off
	s_mov_b32 m0, s72
	v_lshl_add_u64 v[176:177], v[250:251], 0, s[28:29]
	global_load_lds_dwordx4 v[176:177], off
	s_waitcnt vmcnt(6)
	s_barrier
	v_mfma_f32_16x16x32_f16 v[98:101], v[198:201], v[230:233], v[98:101]
	v_mfma_f32_16x16x32_f16 v[102:105], v[198:201], v[238:241], v[102:105]
	v_mfma_f32_16x16x32_f16 v[106:109], v[206:209], v[230:233], v[106:109]
	v_mfma_f32_16x16x32_f16 v[110:113], v[206:209], v[238:241], v[110:113]
	v_mfma_f32_16x16x32_f16 v[114:117], v[214:217], v[230:233], v[114:117]
	v_mfma_f32_16x16x32_f16 v[118:121], v[214:217], v[238:241], v[118:121]
	v_mfma_f32_16x16x32_f16 v[122:125], v[222:225], v[230:233], v[122:125]
	v_mfma_f32_16x16x32_f16 v[126:129], v[222:225], v[238:241], v[126:129]
	v_mfma_f32_16x16x32_f16 v[98:101], v[202:205], v[234:237], v[98:101]
	v_mfma_f32_16x16x32_f16 v[102:105], v[202:205], v[242:245], v[102:105]
	v_mfma_f32_16x16x32_f16 v[106:109], v[210:213], v[234:237], v[106:109]
	v_mfma_f32_16x16x32_f16 v[110:113], v[210:213], v[242:245], v[110:113]
	v_mfma_f32_16x16x32_f16 v[114:117], v[218:221], v[234:237], v[114:117]
	v_mfma_f32_16x16x32_f16 v[118:121], v[218:221], v[242:245], v[118:121]
	v_mfma_f32_16x16x32_f16 v[122:125], v[226:229], v[234:237], v[122:125]
	v_mfma_f32_16x16x32_f16 v[126:129], v[226:229], v[242:245], v[126:129]
	s_barrier
	ds_read_b128 v[176:179], v144
	ds_read_b128 v[180:183], v145
	ds_read_b128 v[184:187], v150
	ds_read_b128 v[188:191], v151
	s_mov_b32 m0, s73
	v_lshl_add_u64 v[230:231], v[192:193], 0, s[28:29]
	global_load_lds_dwordx4 v[230:231], off
	ds_read_b128 v[198:201], v173 offset:32768
	ds_read_b128 v[202:205], v173 offset:33792
	ds_read_b128 v[206:209], v173 offset:34816
	ds_read_b128 v[210:213], v173 offset:35840
	ds_read_b128 v[214:217], v173 offset:36864
	ds_read_b128 v[218:221], v173 offset:37888
	ds_read_b128 v[222:225], v173 offset:38912
	ds_read_b128 v[226:229], v173 offset:39936
	s_mov_b32 m0, s74
	v_lshl_add_u64 v[230:231], v[246:247], 0, s[28:29]
	global_load_lds_dwordx4 v[230:231], off
	s_waitcnt lgkmcnt(8)
	s_barrier
	s_waitcnt lgkmcnt(0)
	v_mfma_f32_16x16x32_f16 v[2:5], v[198:201], v[176:179], v[2:5]
	v_mfma_f32_16x16x32_f16 v[6:9], v[198:201], v[184:187], v[6:9]
	v_mfma_f32_16x16x32_f16 v[10:13], v[206:209], v[176:179], v[10:13]
	v_mfma_f32_16x16x32_f16 v[18:21], v[206:209], v[184:187], v[18:21]
	v_mfma_f32_16x16x32_f16 v[30:33], v[214:217], v[176:179], v[30:33]
	v_mfma_f32_16x16x32_f16 v[42:45], v[214:217], v[184:187], v[42:45]
	v_mfma_f32_16x16x32_f16 v[54:57], v[222:225], v[176:179], v[54:57]
	v_mfma_f32_16x16x32_f16 v[66:69], v[222:225], v[184:187], v[66:69]
	v_mfma_f32_16x16x32_f16 v[2:5], v[202:205], v[180:183], v[2:5]
	v_mfma_f32_16x16x32_f16 v[6:9], v[202:205], v[188:191], v[6:9]
	v_mfma_f32_16x16x32_f16 v[10:13], v[210:213], v[180:183], v[10:13]
	v_mfma_f32_16x16x32_f16 v[18:21], v[210:213], v[188:191], v[18:21]
	v_mfma_f32_16x16x32_f16 v[30:33], v[218:221], v[180:183], v[30:33]
	v_mfma_f32_16x16x32_f16 v[42:45], v[218:221], v[188:191], v[42:45]
	v_mfma_f32_16x16x32_f16 v[54:57], v[226:229], v[180:183], v[54:57]
	v_mfma_f32_16x16x32_f16 v[66:69], v[226:229], v[188:191], v[66:69]
	s_barrier
	s_mov_b32 m0, s75
	v_lshl_add_u64 v[252:253], v[248:249], 0, s[30:31]
	global_load_lds_dwordx4 v[252:253], off
	ds_read_b128 v[230:233], v146
	ds_read_b128 v[234:237], v147
	ds_read_b128 v[238:241], v148
	ds_read_b128 v[242:245], v149
	s_mov_b32 m0, s76
	v_lshl_add_u64 v[252:253], v[250:251], 0, s[30:31]
	global_load_lds_dwordx4 v[252:253], off
	s_barrier
	s_waitcnt lgkmcnt(0)
	v_mfma_f32_16x16x32_f16 v[14:17], v[198:201], v[230:233], v[14:17]
	v_mfma_f32_16x16x32_f16 v[22:25], v[198:201], v[238:241], v[22:25]
	v_mfma_f32_16x16x32_f16 v[34:37], v[206:209], v[230:233], v[34:37]
	v_mfma_f32_16x16x32_f16 v[46:49], v[206:209], v[238:241], v[46:49]
	v_mfma_f32_16x16x32_f16 v[58:61], v[214:217], v[230:233], v[58:61]
	v_mfma_f32_16x16x32_f16 v[70:73], v[214:217], v[238:241], v[70:73]
	v_mfma_f32_16x16x32_f16 v[78:81], v[222:225], v[230:233], v[78:81]
	v_mfma_f32_16x16x32_f16 v[86:89], v[222:225], v[238:241], v[86:89]
	v_mfma_f32_16x16x32_f16 v[14:17], v[202:205], v[234:237], v[14:17]
	v_mfma_f32_16x16x32_f16 v[22:25], v[202:205], v[242:245], v[22:25]
	v_mfma_f32_16x16x32_f16 v[34:37], v[210:213], v[234:237], v[34:37]
	v_mfma_f32_16x16x32_f16 v[46:49], v[210:213], v[242:245], v[46:49]
	v_mfma_f32_16x16x32_f16 v[58:61], v[218:221], v[234:237], v[58:61]
	v_mfma_f32_16x16x32_f16 v[70:73], v[218:221], v[242:245], v[70:73]
	v_mfma_f32_16x16x32_f16 v[78:81], v[226:229], v[234:237], v[78:81]
	v_mfma_f32_16x16x32_f16 v[86:89], v[226:229], v[242:245], v[86:89]
	v_lshl_add_u64 v[192:193], v[192:193], 0, s[30:31]
	s_mov_b32 m0, s77
	s_barrier
	ds_read_b128 v[198:201], v173 offset:49152
	ds_read_b128 v[202:205], v173 offset:50176
	ds_read_b128 v[206:209], v173 offset:51200
	ds_read_b128 v[210:213], v173 offset:52224
	ds_read_b128 v[214:217], v173 offset:53248
	ds_read_b128 v[218:221], v173 offset:54272
	ds_read_b128 v[222:225], v173 offset:55296
	ds_read_b128 v[226:229], v173 offset:56320
	global_load_lds_dwordx4 v[192:193], off
	s_mov_b32 m0, s78
	v_lshl_add_u64 v[192:193], v[246:247], 0, s[30:31]
	global_load_lds_dwordx4 v[192:193], off
	s_barrier
	s_waitcnt lgkmcnt(0)
	v_mfma_f32_16x16x32_f16 v[26:29], v[198:201], v[176:179], v[26:29]
	v_mfma_f32_16x16x32_f16 v[38:41], v[198:201], v[184:187], v[38:41]
	v_mfma_f32_16x16x32_f16 v[50:53], v[206:209], v[176:179], v[50:53]
	v_mfma_f32_16x16x32_f16 v[62:65], v[206:209], v[184:187], v[62:65]
	v_mfma_f32_16x16x32_f16 v[74:77], v[214:217], v[176:179], v[74:77]
	v_mfma_f32_16x16x32_f16 v[82:85], v[214:217], v[184:187], v[82:85]
	v_mfma_f32_16x16x32_f16 v[90:93], v[222:225], v[176:179], v[90:93]
	v_mfma_f32_16x16x32_f16 v[94:97], v[222:225], v[184:187], v[94:97]
	v_mfma_f32_16x16x32_f16 v[26:29], v[202:205], v[180:183], v[26:29]
	v_mfma_f32_16x16x32_f16 v[38:41], v[202:205], v[188:191], v[38:41]
	v_mfma_f32_16x16x32_f16 v[50:53], v[210:213], v[180:183], v[50:53]
	v_mfma_f32_16x16x32_f16 v[62:65], v[210:213], v[188:191], v[62:65]
	v_mfma_f32_16x16x32_f16 v[74:77], v[218:221], v[180:183], v[74:77]
	v_mfma_f32_16x16x32_f16 v[82:85], v[218:221], v[188:191], v[82:85]
	v_mfma_f32_16x16x32_f16 v[90:93], v[226:229], v[180:183], v[90:93]
	v_mfma_f32_16x16x32_f16 v[94:97], v[226:229], v[188:191], v[94:97]
	s_barrier
	s_mov_b32 m0, s79
	v_lshl_add_u64 v[176:177], v[248:249], 0, s[34:35]
	global_load_lds_dwordx4 v[176:177], off
	s_mov_b32 m0, s80
	v_lshl_add_u64 v[176:177], v[250:251], 0, s[34:35]
	global_load_lds_dwordx4 v[176:177], off
	s_waitcnt vmcnt(6)
	s_barrier
	v_mfma_f32_16x16x32_f16 v[98:101], v[198:201], v[230:233], v[98:101]
	v_mfma_f32_16x16x32_f16 v[102:105], v[198:201], v[238:241], v[102:105]
	v_mfma_f32_16x16x32_f16 v[106:109], v[206:209], v[230:233], v[106:109]
	v_mfma_f32_16x16x32_f16 v[110:113], v[206:209], v[238:241], v[110:113]
	v_mfma_f32_16x16x32_f16 v[114:117], v[214:217], v[230:233], v[114:117]
	v_mfma_f32_16x16x32_f16 v[118:121], v[214:217], v[238:241], v[118:121]
	v_mfma_f32_16x16x32_f16 v[122:125], v[222:225], v[230:233], v[122:125]
	v_mfma_f32_16x16x32_f16 v[126:129], v[222:225], v[238:241], v[126:129]
	v_mfma_f32_16x16x32_f16 v[98:101], v[202:205], v[234:237], v[98:101]
	v_mfma_f32_16x16x32_f16 v[102:105], v[202:205], v[242:245], v[102:105]
	v_mfma_f32_16x16x32_f16 v[106:109], v[210:213], v[234:237], v[106:109]
	v_mfma_f32_16x16x32_f16 v[110:113], v[210:213], v[242:245], v[110:113]
	v_mfma_f32_16x16x32_f16 v[114:117], v[218:221], v[234:237], v[114:117]
	v_mfma_f32_16x16x32_f16 v[118:121], v[218:221], v[242:245], v[118:121]
	v_mfma_f32_16x16x32_f16 v[122:125], v[226:229], v[234:237], v[122:125]
	v_mfma_f32_16x16x32_f16 v[126:129], v[226:229], v[242:245], v[126:129]
	s_add_i32 s44, s44, 2
	s_add_u32 s42, s42, 0x100
	s_addc_u32 s43, s43, 0
	s_cmp_lt_u32 s44, 4
	s_barrier
	s_cbranch_scc1 .LBB9_38
	s_add_u32 s40, s40, 0x20380
	s_addc_u32 s41, s41, 0
	v_readfirstlane_b32 s39, v174
	v_lshl_add_u64 v[130:131], v[130:131], 1, s[40:41]
	s_mov_b32 m0, s39
	v_readfirstlane_b32 s39, v175
	ds_read_b128 v[134:137], v169
	ds_read_b128 v[138:141], v170
	ds_read_b128 v[152:155], v171
	ds_read_b128 v[156:159], v172
	ds_read_b128 v[166:169], v173
	ds_read_b128 v[176:179], v173 offset:1024
	ds_read_b128 v[180:183], v173 offset:2048
	ds_read_b128 v[184:187], v173 offset:3072
	ds_read_b128 v[188:191], v173 offset:4096
	ds_read_b128 v[198:201], v173 offset:5120
	ds_read_b128 v[202:205], v173 offset:6144
	ds_read_b128 v[206:209], v173 offset:7168
	global_load_lds_dwordx4 v[130:131], off
	s_mov_b32 m0, s39
	v_lshl_add_u64 v[130:131], v[132:133], 1, s[40:41]
	global_load_lds_dwordx4 v[130:131], off
	s_barrier
	s_waitcnt lgkmcnt(0)
	v_mfma_f32_16x16x32_f16 v[2:5], v[166:169], v[134:137], v[2:5]
	v_mfma_f32_16x16x32_f16 v[6:9], v[166:169], v[152:155], v[6:9]
	v_mfma_f32_16x16x32_f16 v[30:33], v[188:191], v[134:137], v[30:33]
	v_mfma_f32_16x16x32_f16 v[2:5], v[176:179], v[138:141], v[2:5]
	v_mfma_f32_16x16x32_f16 v[6:9], v[176:179], v[156:159], v[6:9]
	v_mfma_f32_16x16x32_f16 v[10:13], v[180:183], v[134:137], v[10:13]
	v_mfma_f32_16x16x32_f16 v[18:21], v[180:183], v[152:155], v[18:21]
	v_mfma_f32_16x16x32_f16 v[30:33], v[198:201], v[138:141], v[30:33]
	v_mfma_f32_16x16x32_f16 v[42:45], v[188:191], v[152:155], v[42:45]
	v_mfma_f32_16x16x32_f16 v[54:57], v[202:205], v[134:137], v[54:57]
	v_mfma_f32_16x16x32_f16 v[66:69], v[202:205], v[152:155], v[66:69]
	v_mfma_f32_16x16x32_f16 v[10:13], v[184:187], v[138:141], v[10:13]
	v_mfma_f32_16x16x32_f16 v[18:21], v[184:187], v[156:159], v[18:21]
	v_mfma_f32_16x16x32_f16 v[42:45], v[198:201], v[156:159], v[42:45]
	v_mfma_f32_16x16x32_f16 v[54:57], v[206:209], v[138:141], v[54:57]
	v_mfma_f32_16x16x32_f16 v[66:69], v[206:209], v[156:159], v[66:69]
	s_barrier
	ds_read_b128 v[130:133], v161
	ds_read_b128 v[210:213], v162
	ds_read_b128 v[160:163], v163
	ds_read_b128 v[214:217], v164
	s_barrier
	s_waitcnt lgkmcnt(0)
	v_mfma_f32_16x16x32_f16 v[58:61], v[188:191], v[130:133], v[58:61]
	v_mfma_f32_16x16x32_f16 v[14:17], v[166:169], v[130:133], v[14:17]
	v_mfma_f32_16x16x32_f16 v[22:25], v[166:169], v[160:163], v[22:25]
	v_mfma_f32_16x16x32_f16 v[164:167], v[198:201], v[210:213], v[58:61]
	v_mfma_f32_16x16x32_f16 v[58:61], v[188:191], v[160:163], v[70:73]
	v_mfma_f32_16x16x32_f16 v[46:49], v[180:183], v[160:163], v[46:49]
	v_mfma_f32_16x16x32_f16 v[168:171], v[198:201], v[214:217], v[58:61]
	v_mfma_f32_16x16x32_f16 v[58:61], v[202:205], v[130:133], v[78:81]
	v_mfma_f32_16x16x32_f16 v[14:17], v[176:179], v[210:213], v[14:17]
	v_mfma_f32_16x16x32_f16 v[34:37], v[180:183], v[130:133], v[34:37]
	v_mfma_f32_16x16x32_f16 v[46:49], v[184:187], v[214:217], v[46:49]
	v_mfma_f32_16x16x32_f16 v[78:81], v[206:209], v[210:213], v[58:61]
	v_mfma_f32_16x16x32_f16 v[58:61], v[202:205], v[160:163], v[86:89]
	v_mfma_f32_16x16x32_f16 v[22:25], v[176:179], v[214:217], v[22:25]
	v_mfma_f32_16x16x32_f16 v[34:37], v[184:187], v[210:213], v[34:37]
	v_mfma_f32_16x16x32_f16 v[86:89], v[206:209], v[214:217], v[58:61]
	s_barrier
	s_nop 2
	ds_read_b128 v[58:61], v173 offset:16384
	ds_read_b128 v[70:73], v173 offset:17408
	ds_read_b128 v[174:177], v173 offset:18432
	ds_read_b128 v[178:181], v173 offset:19456
	ds_read_b128 v[182:185], v173 offset:20480
	ds_read_b128 v[186:189], v173 offset:21504
	ds_read_b128 v[190:193], v173 offset:22528
	ds_read_b128 v[198:201], v173 offset:23552
	s_waitcnt vmcnt(4)
	s_barrier
	s_waitcnt lgkmcnt(0)
	v_mfma_f32_16x16x32_f16 v[26:29], v[58:61], v[134:137], v[26:29]
	v_mfma_f32_16x16x32_f16 v[26:29], v[70:73], v[138:141], v[26:29]
	v_mfma_f32_16x16x32_f16 v[38:41], v[58:61], v[152:155], v[38:41]
	v_mfma_f32_16x16x32_f16 v[50:53], v[174:177], v[134:137], v[50:53]
	v_mfma_f32_16x16x32_f16 v[62:65], v[174:177], v[152:155], v[62:65]
	v_mfma_f32_16x16x32_f16 v[74:77], v[182:185], v[134:137], v[74:77]
	v_mfma_f32_16x16x32_f16 v[82:85], v[182:185], v[152:155], v[82:85]
	v_mfma_f32_16x16x32_f16 v[90:93], v[190:193], v[134:137], v[90:93]
	v_mfma_f32_16x16x32_f16 v[94:97], v[190:193], v[152:155], v[94:97]
	v_mfma_f32_16x16x32_f16 v[38:41], v[70:73], v[156:159], v[38:41]
	v_mfma_f32_16x16x32_f16 v[50:53], v[178:181], v[138:141], v[50:53]
	v_mfma_f32_16x16x32_f16 v[62:65], v[178:181], v[156:159], v[62:65]
	v_mfma_f32_16x16x32_f16 v[74:77], v[186:189], v[138:141], v[74:77]
	v_mfma_f32_16x16x32_f16 v[82:85], v[186:189], v[156:159], v[82:85]
	v_mfma_f32_16x16x32_f16 v[90:93], v[198:201], v[138:141], v[90:93]
	v_mfma_f32_16x16x32_f16 v[94:97], v[198:201], v[156:159], v[94:97]
	v_mfma_f32_16x16x32_f16 v[98:101], v[58:61], v[130:133], v[98:101]
	v_mfma_f32_16x16x32_f16 v[58:61], v[58:61], v[160:163], v[102:105]
	v_mfma_f32_16x16x32_f16 v[102:105], v[70:73], v[214:217], v[58:61]
	v_mfma_f32_16x16x32_f16 v[58:61], v[174:177], v[130:133], v[106:109]
	v_mfma_f32_16x16x32_f16 v[106:109], v[178:181], v[210:213], v[58:61]
	v_mfma_f32_16x16x32_f16 v[58:61], v[174:177], v[160:163], v[110:113]
	v_mfma_f32_16x16x32_f16 v[202:205], v[178:181], v[214:217], v[58:61]
	v_mfma_f32_16x16x32_f16 v[58:61], v[182:185], v[130:133], v[114:117]
	v_mfma_f32_16x16x32_f16 v[206:209], v[186:189], v[210:213], v[58:61]
	v_mfma_f32_16x16x32_f16 v[58:61], v[182:185], v[160:163], v[118:121]
	v_mfma_f32_16x16x32_f16 v[218:221], v[186:189], v[214:217], v[58:61]
	v_mfma_f32_16x16x32_f16 v[58:61], v[190:193], v[130:133], v[122:125]
	v_mfma_f32_16x16x32_f16 v[98:101], v[70:73], v[210:213], v[98:101]
	v_mfma_f32_16x16x32_f16 v[210:213], v[198:201], v[210:213], v[58:61]
	v_mfma_f32_16x16x32_f16 v[58:61], v[190:193], v[160:163], v[126:129]
	v_mfma_f32_16x16x32_f16 v[198:201], v[198:201], v[214:217], v[58:61]
	s_barrier
	ds_read_b128 v[110:113], v144
	ds_read_b128 v[130:133], v145
	ds_read_b128 v[214:217], v150
	ds_read_b128 v[222:225], v151
	s_nop 0
	ds_read_b128 v[58:61], v173 offset:32768
	ds_read_b128 v[70:73], v173 offset:33792
	ds_read_b128 v[114:117], v173 offset:34816
	ds_read_b128 v[118:121], v173 offset:35840
	ds_read_b128 v[134:137], v173 offset:36864
	ds_read_b128 v[138:141], v173 offset:37888
	ds_read_b128 v[178:181], v173 offset:38912
	ds_read_b128 v[226:229], v173 offset:39936
	s_waitcnt vmcnt(2)
	s_barrier
	s_waitcnt lgkmcnt(0)
	v_mfma_f32_16x16x32_f16 v[2:5], v[58:61], v[110:113], v[2:5]
	v_mfma_f32_16x16x32_f16 v[190:193], v[70:73], v[130:133], v[2:5]
	v_mfma_f32_16x16x32_f16 v[2:5], v[58:61], v[214:217], v[6:9]
	v_mfma_f32_16x16x32_f16 v[158:161], v[70:73], v[222:225], v[2:5]
	v_mfma_f32_16x16x32_f16 v[2:5], v[114:117], v[110:113], v[10:13]
	v_mfma_f32_16x16x32_f16 v[186:189], v[118:121], v[130:133], v[2:5]
	v_mfma_f32_16x16x32_f16 v[2:5], v[114:117], v[214:217], v[18:21]
	v_mfma_f32_16x16x32_f16 v[154:157], v[118:121], v[222:225], v[2:5]
	v_mfma_f32_16x16x32_f16 v[2:5], v[134:137], v[110:113], v[30:33]
	v_mfma_f32_16x16x32_f16 v[182:185], v[138:141], v[130:133], v[2:5]
	v_mfma_f32_16x16x32_f16 v[2:5], v[134:137], v[214:217], v[42:45]
	v_mfma_f32_16x16x32_f16 v[150:153], v[138:141], v[222:225], v[2:5]
	v_mfma_f32_16x16x32_f16 v[2:5], v[178:181], v[110:113], v[54:57]
	v_mfma_f32_16x16x32_f16 v[174:177], v[226:229], v[130:133], v[2:5]
	v_mfma_f32_16x16x32_f16 v[2:5], v[178:181], v[214:217], v[66:69]
	v_mfma_f32_16x16x32_f16 v[142:145], v[226:229], v[222:225], v[2:5]
	s_barrier
	s_nop 4
	ds_read_b128 v[2:5], v146
	ds_read_b128 v[10:13], v147
	ds_read_b128 v[18:21], v148
	ds_read_b128 v[42:45], v149
	s_waitcnt vmcnt(0)
	s_barrier
	s_waitcnt lgkmcnt(0)
	v_mfma_f32_16x16x32_f16 v[6:9], v[58:61], v[2:5], v[14:17]
	v_mfma_f32_16x16x32_f16 v[126:129], v[70:73], v[10:13], v[6:9]
	v_mfma_f32_16x16x32_f16 v[6:9], v[58:61], v[18:21], v[22:25]
	v_mfma_f32_16x16x32_f16 v[70:73], v[70:73], v[42:45], v[6:9]
	v_mfma_f32_16x16x32_f16 v[6:9], v[114:117], v[2:5], v[34:37]
	v_mfma_f32_16x16x32_f16 v[122:125], v[118:121], v[10:13], v[6:9]
	v_mfma_f32_16x16x32_f16 v[6:9], v[114:117], v[18:21], v[46:49]
	v_mfma_f32_16x16x32_f16 v[58:61], v[118:121], v[42:45], v[6:9]
	v_mfma_f32_16x16x32_f16 v[6:9], v[134:137], v[2:5], v[164:167]
	v_mfma_f32_16x16x32_f16 v[118:121], v[138:141], v[10:13], v[6:9]
	v_mfma_f32_16x16x32_f16 v[6:9], v[134:137], v[18:21], v[168:171]
	v_mfma_f32_16x16x32_f16 v[46:49], v[138:141], v[42:45], v[6:9]
	v_mfma_f32_16x16x32_f16 v[6:9], v[178:181], v[2:5], v[78:81]
	v_mfma_f32_16x16x32_f16 v[114:117], v[226:229], v[10:13], v[6:9]
	v_mfma_f32_16x16x32_f16 v[6:9], v[178:181], v[18:21], v[86:89]
	v_mfma_f32_16x16x32_f16 v[30:33], v[226:229], v[42:45], v[6:9]
	s_barrier
	s_nop 4
	ds_read_b128 v[6:9], v173 offset:49152
	ds_read_b128 v[14:17], v173 offset:50176
	ds_read_b128 v[22:25], v173 offset:51200
	ds_read_b128 v[34:37], v173 offset:52224
	ds_read_b128 v[54:57], v173 offset:53248
	ds_read_b128 v[66:69], v173 offset:54272
	ds_read_b128 v[78:81], v173 offset:55296
	ds_read_b128 v[86:89], v173 offset:56320
	s_barrier
	s_waitcnt lgkmcnt(0)
	v_mfma_f32_16x16x32_f16 v[26:29], v[6:9], v[110:113], v[26:29]
	v_mfma_f32_16x16x32_f16 v[178:181], v[14:17], v[130:133], v[26:29]
	v_mfma_f32_16x16x32_f16 v[26:29], v[6:9], v[214:217], v[38:41]
	v_mfma_f32_16x16x32_f16 v[146:149], v[14:17], v[222:225], v[26:29]
	v_mfma_f32_16x16x32_f16 v[26:29], v[22:25], v[110:113], v[50:53]
	v_mfma_f32_16x16x32_f16 v[170:173], v[34:37], v[130:133], v[26:29]
	v_mfma_f32_16x16x32_f16 v[26:29], v[22:25], v[214:217], v[62:65]
	v_mfma_f32_16x16x32_f16 v[138:141], v[34:37], v[222:225], v[26:29]
	v_mfma_f32_16x16x32_f16 v[26:29], v[54:57], v[110:113], v[74:77]
	v_mfma_f32_16x16x32_f16 v[166:169], v[66:69], v[130:133], v[26:29]
	v_mfma_f32_16x16x32_f16 v[26:29], v[54:57], v[214:217], v[82:85]
	v_mfma_f32_16x16x32_f16 v[134:137], v[66:69], v[222:225], v[26:29]
	v_mfma_f32_16x16x32_f16 v[26:29], v[78:81], v[110:113], v[90:93]
	v_mfma_f32_16x16x32_f16 v[162:165], v[86:89], v[130:133], v[26:29]
	v_mfma_f32_16x16x32_f16 v[26:29], v[78:81], v[214:217], v[94:97]
	v_mfma_f32_16x16x32_f16 v[130:133], v[86:89], v[222:225], v[26:29]
	v_mfma_f32_16x16x32_f16 v[26:29], v[6:9], v[2:5], v[98:101]
	v_mfma_f32_16x16x32_f16 v[6:9], v[6:9], v[18:21], v[102:105]
	v_mfma_f32_16x16x32_f16 v[110:113], v[14:17], v[10:13], v[26:29]
	v_mfma_f32_16x16x32_f16 v[26:29], v[14:17], v[42:45], v[6:9]
	v_mfma_f32_16x16x32_f16 v[6:9], v[22:25], v[2:5], v[106:109]
	v_mfma_f32_16x16x32_f16 v[106:109], v[34:37], v[10:13], v[6:9]
	v_mfma_f32_16x16x32_f16 v[6:9], v[22:25], v[18:21], v[202:205]
	v_mfma_f32_16x16x32_f16 v[14:17], v[34:37], v[42:45], v[6:9]
	v_mfma_f32_16x16x32_f16 v[6:9], v[54:57], v[2:5], v[206:209]
	v_mfma_f32_16x16x32_f16 v[2:5], v[78:81], v[2:5], v[210:213]
	v_mfma_f32_16x16x32_f16 v[102:105], v[66:69], v[10:13], v[6:9]
	v_mfma_f32_16x16x32_f16 v[6:9], v[54:57], v[18:21], v[218:221]
	v_mfma_f32_16x16x32_f16 v[98:101], v[86:89], v[10:13], v[2:5]
	v_mfma_f32_16x16x32_f16 v[2:5], v[78:81], v[18:21], v[198:201]
	v_mfma_f32_16x16x32_f16 v[6:9], v[66:69], v[42:45], v[6:9]
	v_mfma_f32_16x16x32_f16 v[2:5], v[86:89], v[42:45], v[2:5]
	s_cmpk_gt_u32 s54, 0xff
	s_barrier
	s_cbranch_scc1 .LBB9_34
	s_barrier
	s_branch .LBB9_34

.LBB10_12:
	ds_read_b128 v[182:185], v171
	ds_read_b128 v[186:189], v173
	ds_read_b128 v[190:193], v174
	ds_read_b128 v[194:197], v175
	v_add_u32_e32 v177, 0xc000, v148
	v_lshl_add_u64 v[246:247], v[136:137], 0, s[44:45]
	v_add_u32_e32 v176, s63, v170
	s_mov_b32 m0, s70
	v_lshl_add_u64 v[178:179], v[246:247], 0, s[28:29]
	global_load_lds_dwordx4 v[178:179], off
	ds_read_b128 v[198:201], v176
	ds_read_b128 v[202:205], v176 offset:1024
	ds_read_b128 v[206:209], v176 offset:2048
	ds_read_b128 v[210:213], v176 offset:3072
	ds_read_b128 v[214:217], v176 offset:4096
	ds_read_b128 v[218:221], v176 offset:5120
	ds_read_b128 v[222:225], v176 offset:6144
	ds_read_b128 v[226:229], v176 offset:7168
	v_add_u32_e32 v178, 0xe000, v148
	v_lshl_add_u64 v[248:249], v[134:135], 0, s[44:45]
	s_mov_b32 m0, s71
	v_lshl_add_u64 v[230:231], v[248:249], 0, s[28:29]
	global_load_lds_dwordx4 v[230:231], off
	s_waitcnt lgkmcnt(8)
	s_barrier
	s_waitcnt lgkmcnt(0)
	v_mfma_f32_16x16x32_f16 v[126:129], v[198:201], v[182:185], v[126:129]
	v_mfma_f32_16x16x32_f16 v[122:125], v[198:201], v[190:193], v[122:125]
	v_mfma_f32_16x16x32_f16 v[118:121], v[206:209], v[182:185], v[118:121]
	v_mfma_f32_16x16x32_f16 v[114:117], v[206:209], v[190:193], v[114:117]
	v_mfma_f32_16x16x32_f16 v[110:113], v[214:217], v[182:185], v[110:113]
	v_mfma_f32_16x16x32_f16 v[106:109], v[214:217], v[190:193], v[106:109]
	v_mfma_f32_16x16x32_f16 v[102:105], v[222:225], v[182:185], v[102:105]
	v_mfma_f32_16x16x32_f16 v[98:101], v[222:225], v[190:193], v[98:101]
	v_mfma_f32_16x16x32_f16 v[126:129], v[202:205], v[186:189], v[126:129]
	v_mfma_f32_16x16x32_f16 v[122:125], v[202:205], v[194:197], v[122:125]
	v_mfma_f32_16x16x32_f16 v[118:121], v[210:213], v[186:189], v[118:121]
	v_mfma_f32_16x16x32_f16 v[114:117], v[210:213], v[194:197], v[114:117]
	v_mfma_f32_16x16x32_f16 v[110:113], v[218:221], v[186:189], v[110:113]
	v_mfma_f32_16x16x32_f16 v[106:109], v[218:221], v[194:197], v[106:109]
	v_mfma_f32_16x16x32_f16 v[102:105], v[226:229], v[186:189], v[102:105]
	v_mfma_f32_16x16x32_f16 v[98:101], v[226:229], v[194:197], v[98:101]
	s_barrier
	v_lshl_add_u64 v[250:251], v[140:141], 0, s[44:45]
	s_mov_b32 m0, s72
	v_lshl_add_u64 v[252:253], v[250:251], 0, s[30:31]
	global_load_lds_dwordx4 v[252:253], off
	ds_read_b128 v[230:233], v162
	ds_read_b128 v[234:237], v163
	ds_read_b128 v[238:241], v164
	ds_read_b128 v[242:245], v165
	v_lshl_add_u64 v[252:253], v[138:139], 0, s[44:45]
	s_mov_b32 m0, s73
	v_lshl_add_u64 v[254:255], v[252:253], 0, s[30:31]
	global_load_lds_dwordx4 v[254:255], off
	s_barrier
	s_waitcnt lgkmcnt(0)
	v_mfma_f32_16x16x32_f16 v[94:97], v[198:201], v[230:233], v[94:97]
	v_mfma_f32_16x16x32_f16 v[90:93], v[198:201], v[238:241], v[90:93]
	v_mfma_f32_16x16x32_f16 v[86:89], v[206:209], v[230:233], v[86:89]
	v_mfma_f32_16x16x32_f16 v[82:85], v[206:209], v[238:241], v[82:85]
	v_mfma_f32_16x16x32_f16 v[78:81], v[214:217], v[230:233], v[78:81]
	v_mfma_f32_16x16x32_f16 v[74:77], v[214:217], v[238:241], v[74:77]
	v_mfma_f32_16x16x32_f16 v[70:73], v[222:225], v[230:233], v[70:73]
	v_mfma_f32_16x16x32_f16 v[66:69], v[222:225], v[238:241], v[66:69]
	v_mfma_f32_16x16x32_f16 v[94:97], v[202:205], v[234:237], v[94:97]
	v_mfma_f32_16x16x32_f16 v[90:93], v[202:205], v[242:245], v[90:93]
	v_mfma_f32_16x16x32_f16 v[86:89], v[210:213], v[234:237], v[86:89]
	v_mfma_f32_16x16x32_f16 v[82:85], v[210:213], v[242:245], v[82:85]
	v_mfma_f32_16x16x32_f16 v[78:81], v[218:221], v[234:237], v[78:81]
	v_mfma_f32_16x16x32_f16 v[74:77], v[218:221], v[242:245], v[74:77]
	v_mfma_f32_16x16x32_f16 v[70:73], v[226:229], v[234:237], v[70:73]
	v_mfma_f32_16x16x32_f16 v[66:69], v[226:229], v[242:245], v[66:69]
	v_lshl_add_u64 v[254:255], v[246:247], 0, s[30:31]
	s_mov_b32 m0, s74
	s_barrier
	ds_read_b128 v[198:201], v176 offset:16384
	ds_read_b128 v[202:205], v176 offset:17408
	ds_read_b128 v[206:209], v176 offset:18432
	ds_read_b128 v[210:213], v176 offset:19456
	ds_read_b128 v[214:217], v176 offset:20480
	ds_read_b128 v[218:221], v176 offset:21504
	ds_read_b128 v[222:225], v176 offset:22528
	ds_read_b128 v[226:229], v176 offset:23552
	global_load_lds_dwordx4 v[254:255], off
	s_mov_b32 m0, s75
	v_lshl_add_u64 v[254:255], v[248:249], 0, s[30:31]
	global_load_lds_dwordx4 v[254:255], off
	s_barrier
	s_waitcnt lgkmcnt(0)
	v_mfma_f32_16x16x32_f16 v[62:65], v[198:201], v[182:185], v[62:65]
	v_mfma_f32_16x16x32_f16 v[58:61], v[198:201], v[190:193], v[58:61]
	v_mfma_f32_16x16x32_f16 v[54:57], v[206:209], v[182:185], v[54:57]
	v_mfma_f32_16x16x32_f16 v[50:53], v[206:209], v[190:193], v[50:53]
	v_mfma_f32_16x16x32_f16 v[46:49], v[214:217], v[182:185], v[46:49]
	v_mfma_f32_16x16x32_f16 v[42:45], v[214:217], v[190:193], v[42:45]
	v_mfma_f32_16x16x32_f16 v[38:41], v[222:225], v[182:185], v[38:41]
	v_mfma_f32_16x16x32_f16 v[34:37], v[222:225], v[190:193], v[34:37]
	v_mfma_f32_16x16x32_f16 v[62:65], v[202:205], v[186:189], v[62:65]
	v_mfma_f32_16x16x32_f16 v[58:61], v[202:205], v[194:197], v[58:61]
	v_mfma_f32_16x16x32_f16 v[54:57], v[210:213], v[186:189], v[54:57]
	v_mfma_f32_16x16x32_f16 v[50:53], v[210:213], v[194:197], v[50:53]
	v_mfma_f32_16x16x32_f16 v[46:49], v[218:221], v[186:189], v[46:49]
	v_mfma_f32_16x16x32_f16 v[42:45], v[218:221], v[194:197], v[42:45]
	v_mfma_f32_16x16x32_f16 v[38:41], v[226:229], v[186:189], v[38:41]
	v_mfma_f32_16x16x32_f16 v[34:37], v[226:229], v[194:197], v[34:37]
	s_barrier
	s_mov_b32 m0, s76
	v_lshl_add_u64 v[182:183], v[250:251], 0, s[34:35]
	global_load_lds_dwordx4 v[182:183], off
	s_mov_b32 m0, s77
	v_lshl_add_u64 v[182:183], v[252:253], 0, s[34:35]
	global_load_lds_dwordx4 v[182:183], off
	s_waitcnt vmcnt(6)
	s_barrier
	v_mfma_f32_16x16x32_f16 v[30:33], v[198:201], v[230:233], v[30:33]
	v_mfma_f32_16x16x32_f16 v[26:29], v[198:201], v[238:241], v[26:29]
	v_mfma_f32_16x16x32_f16 v[22:25], v[206:209], v[230:233], v[22:25]
	v_mfma_f32_16x16x32_f16 v[18:21], v[206:209], v[238:241], v[18:21]
	v_mfma_f32_16x16x32_f16 v[14:17], v[214:217], v[230:233], v[14:17]
	v_mfma_f32_16x16x32_f16 v[10:13], v[214:217], v[238:241], v[10:13]
	v_mfma_f32_16x16x32_f16 v[6:9], v[222:225], v[230:233], v[6:9]
	v_mfma_f32_16x16x32_f16 v[2:5], v[222:225], v[238:241], v[2:5]
	v_mfma_f32_16x16x32_f16 v[30:33], v[202:205], v[234:237], v[30:33]
	v_mfma_f32_16x16x32_f16 v[26:29], v[202:205], v[242:245], v[26:29]
	v_mfma_f32_16x16x32_f16 v[22:25], v[210:213], v[234:237], v[22:25]
	v_mfma_f32_16x16x32_f16 v[18:21], v[210:213], v[242:245], v[18:21]
	v_mfma_f32_16x16x32_f16 v[14:17], v[218:221], v[234:237], v[14:17]
	v_mfma_f32_16x16x32_f16 v[10:13], v[218:221], v[242:245], v[10:13]
	v_mfma_f32_16x16x32_f16 v[6:9], v[226:229], v[234:237], v[6:9]
	v_mfma_f32_16x16x32_f16 v[2:5], v[226:229], v[242:245], v[2:5]
	s_barrier
	ds_read_b128 v[182:185], v144
	ds_read_b128 v[186:189], v145
	ds_read_b128 v[190:193], v146
	ds_read_b128 v[194:197], v147
	s_mov_b32 m0, s78
	v_lshl_add_u64 v[230:231], v[246:247], 0, s[34:35]
	global_load_lds_dwordx4 v[230:231], off
	ds_read_b128 v[198:201], v176 offset:32768
	ds_read_b128 v[202:205], v176 offset:33792
	ds_read_b128 v[206:209], v176 offset:34816
	ds_read_b128 v[210:213], v176 offset:35840
	ds_read_b128 v[214:217], v176 offset:36864
	ds_read_b128 v[218:221], v176 offset:37888
	ds_read_b128 v[222:225], v176 offset:38912
	ds_read_b128 v[226:229], v176 offset:39936
	s_mov_b32 m0, s79
	v_lshl_add_u64 v[230:231], v[248:249], 0, s[34:35]
	global_load_lds_dwordx4 v[230:231], off
	s_waitcnt lgkmcnt(8)
	s_barrier
	s_waitcnt lgkmcnt(0)
	v_mfma_f32_16x16x32_f16 v[126:129], v[198:201], v[182:185], v[126:129]
	v_mfma_f32_16x16x32_f16 v[122:125], v[198:201], v[190:193], v[122:125]
	v_mfma_f32_16x16x32_f16 v[118:121], v[206:209], v[182:185], v[118:121]
	v_mfma_f32_16x16x32_f16 v[114:117], v[206:209], v[190:193], v[114:117]
	v_mfma_f32_16x16x32_f16 v[110:113], v[214:217], v[182:185], v[110:113]
	v_mfma_f32_16x16x32_f16 v[106:109], v[214:217], v[190:193], v[106:109]
	v_mfma_f32_16x16x32_f16 v[102:105], v[222:225], v[182:185], v[102:105]
	v_mfma_f32_16x16x32_f16 v[98:101], v[222:225], v[190:193], v[98:101]
	v_mfma_f32_16x16x32_f16 v[126:129], v[202:205], v[186:189], v[126:129]
	v_mfma_f32_16x16x32_f16 v[122:125], v[202:205], v[194:197], v[122:125]
	v_mfma_f32_16x16x32_f16 v[118:121], v[210:213], v[186:189], v[118:121]
	v_mfma_f32_16x16x32_f16 v[114:117], v[210:213], v[194:197], v[114:117]
	v_mfma_f32_16x16x32_f16 v[110:113], v[218:221], v[186:189], v[110:113]
	v_mfma_f32_16x16x32_f16 v[106:109], v[218:221], v[194:197], v[106:109]
	v_mfma_f32_16x16x32_f16 v[102:105], v[226:229], v[186:189], v[102:105]
	v_mfma_f32_16x16x32_f16 v[98:101], v[226:229], v[194:197], v[98:101]
	s_barrier
	s_mov_b32 m0, s80
	v_lshl_add_u64 v[254:255], v[250:251], 0, s[36:37]
	global_load_lds_dwordx4 v[254:255], off
	ds_read_b128 v[230:233], v150
	ds_read_b128 v[234:237], v151
	ds_read_b128 v[238:241], v152
	ds_read_b128 v[242:245], v153
	s_mov_b32 m0, s81
	v_lshl_add_u64 v[254:255], v[252:253], 0, s[36:37]
	global_load_lds_dwordx4 v[254:255], off
	s_barrier
	s_waitcnt lgkmcnt(0)
	v_mfma_f32_16x16x32_f16 v[94:97], v[198:201], v[230:233], v[94:97]
	v_mfma_f32_16x16x32_f16 v[90:93], v[198:201], v[238:241], v[90:93]
	v_mfma_f32_16x16x32_f16 v[86:89], v[206:209], v[230:233], v[86:89]
	v_mfma_f32_16x16x32_f16 v[82:85], v[206:209], v[238:241], v[82:85]
	v_mfma_f32_16x16x32_f16 v[78:81], v[214:217], v[230:233], v[78:81]
	v_mfma_f32_16x16x32_f16 v[74:77], v[214:217], v[238:241], v[74:77]
	v_mfma_f32_16x16x32_f16 v[70:73], v[222:225], v[230:233], v[70:73]
	v_mfma_f32_16x16x32_f16 v[66:69], v[222:225], v[238:241], v[66:69]
	v_mfma_f32_16x16x32_f16 v[94:97], v[202:205], v[234:237], v[94:97]
	v_mfma_f32_16x16x32_f16 v[90:93], v[202:205], v[242:245], v[90:93]
	v_mfma_f32_16x16x32_f16 v[86:89], v[210:213], v[234:237], v[86:89]
	v_mfma_f32_16x16x32_f16 v[82:85], v[210:213], v[242:245], v[82:85]
	v_mfma_f32_16x16x32_f16 v[78:81], v[218:221], v[234:237], v[78:81]
	v_mfma_f32_16x16x32_f16 v[74:77], v[218:221], v[242:245], v[74:77]
	v_mfma_f32_16x16x32_f16 v[70:73], v[226:229], v[234:237], v[70:73]
	v_mfma_f32_16x16x32_f16 v[66:69], v[226:229], v[242:245], v[66:69]
	v_lshl_add_u64 v[246:247], v[246:247], 0, s[36:37]
	s_mov_b32 m0, s82
	s_barrier
	ds_read_b128 v[198:201], v176 offset:49152
	ds_read_b128 v[202:205], v176 offset:50176
	ds_read_b128 v[206:209], v176 offset:51200
	ds_read_b128 v[210:213], v176 offset:52224
	ds_read_b128 v[214:217], v176 offset:53248
	ds_read_b128 v[218:221], v176 offset:54272
	ds_read_b128 v[222:225], v176 offset:55296
	ds_read_b128 v[226:229], v176 offset:56320
	global_load_lds_dwordx4 v[246:247], off
	s_mov_b32 m0, s83
	v_lshl_add_u64 v[246:247], v[248:249], 0, s[36:37]
	global_load_lds_dwordx4 v[246:247], off
	s_barrier
	s_waitcnt lgkmcnt(0)
	v_mfma_f32_16x16x32_f16 v[62:65], v[198:201], v[182:185], v[62:65]
	v_mfma_f32_16x16x32_f16 v[58:61], v[198:201], v[190:193], v[58:61]
	v_mfma_f32_16x16x32_f16 v[54:57], v[206:209], v[182:185], v[54:57]
	v_mfma_f32_16x16x32_f16 v[50:53], v[206:209], v[190:193], v[50:53]
	v_mfma_f32_16x16x32_f16 v[46:49], v[214:217], v[182:185], v[46:49]
	v_mfma_f32_16x16x32_f16 v[42:45], v[214:217], v[190:193], v[42:45]
	v_mfma_f32_16x16x32_f16 v[38:41], v[222:225], v[182:185], v[38:41]
	v_mfma_f32_16x16x32_f16 v[34:37], v[222:225], v[190:193], v[34:37]
	v_mfma_f32_16x16x32_f16 v[62:65], v[202:205], v[186:189], v[62:65]
	v_mfma_f32_16x16x32_f16 v[58:61], v[202:205], v[194:197], v[58:61]
	v_mfma_f32_16x16x32_f16 v[54:57], v[210:213], v[186:189], v[54:57]
	v_mfma_f32_16x16x32_f16 v[50:53], v[210:213], v[194:197], v[50:53]
	v_mfma_f32_16x16x32_f16 v[46:49], v[218:221], v[186:189], v[46:49]
	v_mfma_f32_16x16x32_f16 v[42:45], v[218:221], v[194:197], v[42:45]
	v_mfma_f32_16x16x32_f16 v[38:41], v[226:229], v[186:189], v[38:41]
	v_mfma_f32_16x16x32_f16 v[34:37], v[226:229], v[194:197], v[34:37]
	s_barrier
	s_mov_b32 m0, s84
	v_lshl_add_u64 v[182:183], v[250:251], 0, s[38:39]
	global_load_lds_dwordx4 v[182:183], off
	s_mov_b32 m0, s85
	v_lshl_add_u64 v[182:183], v[252:253], 0, s[38:39]
	global_load_lds_dwordx4 v[182:183], off
	s_waitcnt vmcnt(6)
	s_barrier
	v_mfma_f32_16x16x32_f16 v[30:33], v[198:201], v[230:233], v[30:33]
	v_mfma_f32_16x16x32_f16 v[26:29], v[198:201], v[238:241], v[26:29]
	v_mfma_f32_16x16x32_f16 v[22:25], v[206:209], v[230:233], v[22:25]
	v_mfma_f32_16x16x32_f16 v[18:21], v[206:209], v[238:241], v[18:21]
	v_mfma_f32_16x16x32_f16 v[14:17], v[214:217], v[230:233], v[14:17]
	v_mfma_f32_16x16x32_f16 v[10:13], v[214:217], v[238:241], v[10:13]
	v_mfma_f32_16x16x32_f16 v[6:9], v[222:225], v[230:233], v[6:9]
	v_mfma_f32_16x16x32_f16 v[2:5], v[222:225], v[238:241], v[2:5]
	v_mfma_f32_16x16x32_f16 v[30:33], v[202:205], v[234:237], v[30:33]
	v_mfma_f32_16x16x32_f16 v[26:29], v[202:205], v[242:245], v[26:29]
	v_mfma_f32_16x16x32_f16 v[22:25], v[210:213], v[234:237], v[22:25]
	v_mfma_f32_16x16x32_f16 v[18:21], v[210:213], v[242:245], v[18:21]
	v_mfma_f32_16x16x32_f16 v[14:17], v[218:221], v[234:237], v[14:17]
	v_mfma_f32_16x16x32_f16 v[10:13], v[218:221], v[242:245], v[10:13]
	v_mfma_f32_16x16x32_f16 v[6:9], v[226:229], v[234:237], v[6:9]
	v_mfma_f32_16x16x32_f16 v[2:5], v[226:229], v[242:245], v[2:5]
	s_add_i32 s46, s46, 2
	s_add_u32 s44, s44, 0x100
	s_addc_u32 s45, s45, 0
	s_cmp_lt_u32 s46, 28
	s_barrier
	s_cbranch_scc1 .LBB10_12
	s_add_u32 s42, s42, 0x80f80
	s_addc_u32 s43, s43, 0
	v_readfirstlane_b32 s44, v177
	v_lshl_add_u64 v[130:131], v[130:131], 1, s[42:43]
	s_mov_b32 m0, s44
	ds_read_b128 v[134:137], v171
	ds_read_b128 v[138:141], v173
	ds_read_b128 v[154:157], v174
	ds_read_b128 v[168:171], v175
	ds_read_b128 v[182:185], v176
	ds_read_b128 v[186:189], v176 offset:1024
	ds_read_b128 v[190:193], v176 offset:2048
	ds_read_b128 v[194:197], v176 offset:3072
	ds_read_b128 v[198:201], v176 offset:4096
	ds_read_b128 v[202:205], v176 offset:5120
	ds_read_b128 v[206:209], v176 offset:6144
	ds_read_b128 v[210:213], v176 offset:7168
	global_load_lds_dwordx4 v[130:131], off
	v_lshl_add_u64 v[130:131], v[132:133], 1, s[42:43]
	v_readfirstlane_b32 s42, v178
	s_mov_b32 m0, s42
	s_nop 0
	global_load_lds_dwordx4 v[130:131], off
	s_barrier
	s_waitcnt lgkmcnt(0)
	v_mfma_f32_16x16x32_f16 v[122:125], v[182:185], v[154:157], v[122:125]
	v_mfma_f32_16x16x32_f16 v[110:113], v[198:201], v[134:137], v[110:113]
	v_mfma_f32_16x16x32_f16 v[98:101], v[206:209], v[154:157], v[98:101]
	v_mfma_f32_16x16x32_f16 v[126:129], v[182:185], v[134:137], v[126:129]
	v_mfma_f32_16x16x32_f16 v[122:125], v[186:189], v[168:171], v[122:125]
	v_mfma_f32_16x16x32_f16 v[118:121], v[190:193], v[134:137], v[118:121]
	v_mfma_f32_16x16x32_f16 v[114:117], v[190:193], v[154:157], v[114:117]
	v_mfma_f32_16x16x32_f16 v[130:133], v[202:205], v[138:141], v[110:113]
	v_mfma_f32_16x16x32_f16 v[106:109], v[198:201], v[154:157], v[106:109]
	v_mfma_f32_16x16x32_f16 v[102:105], v[206:209], v[134:137], v[102:105]
	v_mfma_f32_16x16x32_f16 v[98:101], v[210:213], v[168:171], v[98:101]
	v_mfma_f32_16x16x32_f16 v[126:129], v[186:189], v[138:141], v[126:129]
	v_mfma_f32_16x16x32_f16 v[118:121], v[194:197], v[138:141], v[118:121]
	v_mfma_f32_16x16x32_f16 v[114:117], v[194:197], v[168:171], v[114:117]
	v_mfma_f32_16x16x32_f16 v[214:217], v[202:205], v[168:171], v[106:109]
	v_mfma_f32_16x16x32_f16 v[102:105], v[210:213], v[138:141], v[102:105]
	s_barrier
	ds_read_b128 v[106:109], v162
	ds_read_b128 v[110:113], v163
	ds_read_b128 v[160:163], v164
	ds_read_b128 v[218:221], v165
	s_barrier
	s_waitcnt lgkmcnt(0)
	v_mfma_f32_16x16x32_f16 v[82:85], v[190:193], v[160:163], v[82:85]
	v_mfma_f32_16x16x32_f16 v[78:81], v[198:201], v[106:109], v[78:81]
	v_mfma_f32_16x16x32_f16 v[74:77], v[198:201], v[160:163], v[74:77]
	v_mfma_f32_16x16x32_f16 v[70:73], v[206:209], v[106:109], v[70:73]
	v_mfma_f32_16x16x32_f16 v[66:69], v[206:209], v[160:163], v[66:69]
	v_mfma_f32_16x16x32_f16 v[94:97], v[182:185], v[106:109], v[94:97]
	v_mfma_f32_16x16x32_f16 v[90:93], v[182:185], v[160:163], v[90:93]
	v_mfma_f32_16x16x32_f16 v[86:89], v[190:193], v[106:109], v[86:89]
	v_mfma_f32_16x16x32_f16 v[82:85], v[194:197], v[218:221], v[82:85]
	v_mfma_f32_16x16x32_f16 v[78:81], v[202:205], v[110:113], v[78:81]
	v_mfma_f32_16x16x32_f16 v[74:77], v[202:205], v[218:221], v[74:77]
	v_mfma_f32_16x16x32_f16 v[70:73], v[210:213], v[110:113], v[70:73]
	v_mfma_f32_16x16x32_f16 v[66:69], v[210:213], v[218:221], v[66:69]
	v_mfma_f32_16x16x32_f16 v[222:225], v[186:189], v[110:113], v[94:97]
	v_mfma_f32_16x16x32_f16 v[182:185], v[186:189], v[218:221], v[90:93]
	v_mfma_f32_16x16x32_f16 v[86:89], v[194:197], v[110:113], v[86:89]
	s_barrier
	ds_read_b128 v[90:93], v176 offset:16384
	ds_read_b128 v[94:97], v176 offset:17408
	ds_read_b128 v[186:189], v176 offset:18432
	ds_read_b128 v[190:193], v176 offset:19456
	ds_read_b128 v[194:197], v176 offset:20480
	ds_read_b128 v[198:201], v176 offset:21504
	ds_read_b128 v[202:205], v176 offset:22528
	ds_read_b128 v[206:209], v176 offset:23552
	s_waitcnt vmcnt(4)
	s_barrier
	s_waitcnt lgkmcnt(0)
	v_mfma_f32_16x16x32_f16 v[46:49], v[194:197], v[134:137], v[46:49]
	v_mfma_f32_16x16x32_f16 v[42:45], v[194:197], v[154:157], v[42:45]
	v_mfma_f32_16x16x32_f16 v[38:41], v[202:205], v[134:137], v[38:41]
	v_mfma_f32_16x16x32_f16 v[34:37], v[202:205], v[154:157], v[34:37]
	v_mfma_f32_16x16x32_f16 v[62:65], v[90:93], v[134:137], v[62:65]
	v_mfma_f32_16x16x32_f16 v[58:61], v[90:93], v[154:157], v[58:61]
	v_mfma_f32_16x16x32_f16 v[54:57], v[186:189], v[134:137], v[54:57]
	v_mfma_f32_16x16x32_f16 v[50:53], v[186:189], v[154:157], v[50:53]
	v_mfma_f32_16x16x32_f16 v[46:49], v[198:201], v[138:141], v[46:49]
	v_mfma_f32_16x16x32_f16 v[42:45], v[198:201], v[168:171], v[42:45]
	v_mfma_f32_16x16x32_f16 v[38:41], v[206:209], v[138:141], v[38:41]
	v_mfma_f32_16x16x32_f16 v[34:37], v[206:209], v[168:171], v[34:37]
	v_mfma_f32_16x16x32_f16 v[210:213], v[94:97], v[138:141], v[62:65]
	v_mfma_f32_16x16x32_f16 v[226:229], v[94:97], v[168:171], v[58:61]
	v_mfma_f32_16x16x32_f16 v[230:233], v[190:193], v[138:141], v[54:57]
	v_mfma_f32_16x16x32_f16 v[234:237], v[190:193], v[168:171], v[50:53]
	v_mfma_f32_16x16x32_f16 v[2:5], v[202:205], v[160:163], v[2:5]
	v_mfma_f32_16x16x32_f16 v[30:33], v[90:93], v[106:109], v[30:33]
	v_mfma_f32_16x16x32_f16 v[26:29], v[90:93], v[160:163], v[26:29]
	v_mfma_f32_16x16x32_f16 v[22:25], v[186:189], v[106:109], v[22:25]
	v_mfma_f32_16x16x32_f16 v[18:21], v[186:189], v[160:163], v[18:21]
	v_mfma_f32_16x16x32_f16 v[14:17], v[194:197], v[106:109], v[14:17]
	v_mfma_f32_16x16x32_f16 v[10:13], v[194:197], v[160:163], v[10:13]
	v_mfma_f32_16x16x32_f16 v[6:9], v[202:205], v[106:109], v[6:9]
	v_mfma_f32_16x16x32_f16 v[2:5], v[206:209], v[218:221], v[2:5]
	v_mfma_f32_16x16x32_f16 v[138:141], v[94:97], v[110:113], v[30:33]
	v_mfma_f32_16x16x32_f16 v[168:171], v[94:97], v[218:221], v[26:29]
	v_mfma_f32_16x16x32_f16 v[238:241], v[190:193], v[110:113], v[22:25]
	v_mfma_f32_16x16x32_f16 v[186:189], v[190:193], v[218:221], v[18:21]
	v_mfma_f32_16x16x32_f16 v[190:193], v[198:201], v[110:113], v[14:17]
	v_mfma_f32_16x16x32_f16 v[194:197], v[198:201], v[218:221], v[10:13]
	v_mfma_f32_16x16x32_f16 v[198:201], v[206:209], v[110:113], v[6:9]
	s_barrier
	s_nop 0
	ds_read_b128 v[6:9], v144
	ds_read_b128 v[10:13], v145
	ds_read_b128 v[14:17], v146
	ds_read_b128 v[160:163], v147
	ds_read_b128 v[18:21], v176 offset:32768
	ds_read_b128 v[22:25], v176 offset:33792
	ds_read_b128 v[26:29], v176 offset:34816
	ds_read_b128 v[50:53], v176 offset:35840
	ds_read_b128 v[202:205], v176 offset:36864
	ds_read_b128 v[206:209], v176 offset:37888
	ds_read_b128 v[218:221], v176 offset:38912
	ds_read_b128 v[242:245], v176 offset:39936
	s_waitcnt vmcnt(2)
	s_barrier
	s_waitcnt lgkmcnt(0)
	v_mfma_f32_16x16x32_f16 v[30:33], v[18:21], v[6:9], v[126:129]
	v_mfma_f32_16x16x32_f16 v[154:157], v[22:25], v[10:13], v[30:33]
	v_mfma_f32_16x16x32_f16 v[30:33], v[18:21], v[14:17], v[122:125]
	v_mfma_f32_16x16x32_f16 v[110:113], v[22:25], v[160:163], v[30:33]
	v_mfma_f32_16x16x32_f16 v[30:33], v[26:29], v[6:9], v[118:121]
	v_mfma_f32_16x16x32_f16 v[146:149], v[50:53], v[10:13], v[30:33]
	v_mfma_f32_16x16x32_f16 v[30:33], v[26:29], v[14:17], v[114:117]
	v_mfma_f32_16x16x32_f16 v[106:109], v[50:53], v[160:163], v[30:33]
	v_mfma_f32_16x16x32_f16 v[30:33], v[202:205], v[6:9], v[130:133]
	v_mfma_f32_16x16x32_f16 v[142:145], v[206:209], v[10:13], v[30:33]
	v_mfma_f32_16x16x32_f16 v[30:33], v[202:205], v[14:17], v[214:217]
	v_mfma_f32_16x16x32_f16 v[94:97], v[206:209], v[160:163], v[30:33]
	v_mfma_f32_16x16x32_f16 v[30:33], v[218:221], v[6:9], v[102:105]
	v_mfma_f32_16x16x32_f16 v[134:137], v[242:245], v[10:13], v[30:33]
	v_mfma_f32_16x16x32_f16 v[30:33], v[218:221], v[14:17], v[98:101]
	v_mfma_f32_16x16x32_f16 v[90:93], v[242:245], v[160:163], v[30:33]
	s_barrier
	ds_read_b128 v[102:105], v150
	ds_read_b128 v[114:117], v151
	ds_read_b128 v[118:121], v152
	ds_read_b128 v[126:129], v153
	s_waitcnt vmcnt(0)
	s_barrier
	s_waitcnt lgkmcnt(0)
	v_mfma_f32_16x16x32_f16 v[30:33], v[18:21], v[102:105], v[222:225]
	v_mfma_f32_16x16x32_f16 v[18:21], v[18:21], v[118:121], v[182:185]
	v_mfma_f32_16x16x32_f16 v[62:65], v[22:25], v[114:117], v[30:33]
	v_mfma_f32_16x16x32_f16 v[30:33], v[22:25], v[126:129], v[18:21]
	v_mfma_f32_16x16x32_f16 v[18:21], v[26:29], v[102:105], v[86:89]
	v_mfma_f32_16x16x32_f16 v[58:61], v[50:53], v[114:117], v[18:21]
	v_mfma_f32_16x16x32_f16 v[18:21], v[26:29], v[118:121], v[82:85]
	v_mfma_f32_16x16x32_f16 v[26:29], v[50:53], v[126:129], v[18:21]
	v_mfma_f32_16x16x32_f16 v[18:21], v[202:205], v[102:105], v[78:81]
	v_mfma_f32_16x16x32_f16 v[54:57], v[206:209], v[114:117], v[18:21]
	v_mfma_f32_16x16x32_f16 v[18:21], v[202:205], v[118:121], v[74:77]
	v_mfma_f32_16x16x32_f16 v[22:25], v[206:209], v[126:129], v[18:21]
	v_mfma_f32_16x16x32_f16 v[18:21], v[218:221], v[102:105], v[70:73]
	v_mfma_f32_16x16x32_f16 v[50:53], v[242:245], v[114:117], v[18:21]
	v_mfma_f32_16x16x32_f16 v[18:21], v[218:221], v[118:121], v[66:69]
	v_mfma_f32_16x16x32_f16 v[18:21], v[242:245], v[126:129], v[18:21]
	s_barrier
	ds_read_b128 v[86:89], v176 offset:49152
	ds_read_b128 v[150:153], v176 offset:50176
	ds_read_b128 v[182:185], v176 offset:51200
	ds_read_b128 v[202:205], v176 offset:52224
	ds_read_b128 v[206:209], v176 offset:53248
	ds_read_b128 v[214:217], v176 offset:54272
	ds_read_b128 v[218:221], v176 offset:55296
	ds_read_b128 v[174:177], v176 offset:56320
	s_barrier
	s_waitcnt lgkmcnt(0)
	v_mfma_f32_16x16x32_f16 v[66:69], v[86:89], v[6:9], v[210:213]
	v_mfma_f32_16x16x32_f16 v[130:133], v[150:153], v[10:13], v[66:69]
	v_mfma_f32_16x16x32_f16 v[66:69], v[86:89], v[14:17], v[226:229]
	v_mfma_f32_16x16x32_f16 v[78:81], v[150:153], v[160:163], v[66:69]
	v_mfma_f32_16x16x32_f16 v[66:69], v[182:185], v[6:9], v[230:233]
	v_mfma_f32_16x16x32_f16 v[46:49], v[206:209], v[6:9], v[46:49]
	v_mfma_f32_16x16x32_f16 v[6:9], v[218:221], v[6:9], v[38:41]
	v_mfma_f32_16x16x32_f16 v[122:125], v[202:205], v[10:13], v[66:69]
	v_mfma_f32_16x16x32_f16 v[66:69], v[182:185], v[14:17], v[234:237]
	v_mfma_f32_16x16x32_f16 v[42:45], v[206:209], v[14:17], v[42:45]
	v_mfma_f32_16x16x32_f16 v[82:85], v[174:177], v[10:13], v[6:9]
	v_mfma_f32_16x16x32_f16 v[6:9], v[218:221], v[14:17], v[34:37]
	v_mfma_f32_16x16x32_f16 v[74:77], v[202:205], v[160:163], v[66:69]
	v_mfma_f32_16x16x32_f16 v[98:101], v[214:217], v[10:13], v[46:49]
	v_mfma_f32_16x16x32_f16 v[70:73], v[214:217], v[160:163], v[42:45]
	v_mfma_f32_16x16x32_f16 v[66:69], v[174:177], v[160:163], v[6:9]
	v_mfma_f32_16x16x32_f16 v[6:9], v[86:89], v[102:105], v[138:141]
	v_mfma_f32_16x16x32_f16 v[46:49], v[150:153], v[114:117], v[6:9]
	v_mfma_f32_16x16x32_f16 v[6:9], v[86:89], v[118:121], v[168:171]
	v_mfma_f32_16x16x32_f16 v[14:17], v[150:153], v[126:129], v[6:9]
	v_mfma_f32_16x16x32_f16 v[6:9], v[182:185], v[102:105], v[238:241]
	v_mfma_f32_16x16x32_f16 v[42:45], v[202:205], v[114:117], v[6:9]
	v_mfma_f32_16x16x32_f16 v[6:9], v[182:185], v[118:121], v[186:189]
	v_mfma_f32_16x16x32_f16 v[10:13], v[202:205], v[126:129], v[6:9]
	v_mfma_f32_16x16x32_f16 v[6:9], v[206:209], v[102:105], v[190:193]
	v_mfma_f32_16x16x32_f16 v[38:41], v[214:217], v[114:117], v[6:9]
	v_mfma_f32_16x16x32_f16 v[6:9], v[206:209], v[118:121], v[194:197]
	v_mfma_f32_16x16x32_f16 v[34:37], v[218:221], v[102:105], v[198:201]
	v_mfma_f32_16x16x32_f16 v[2:5], v[218:221], v[118:121], v[2:5]
	v_mfma_f32_16x16x32_f16 v[6:9], v[214:217], v[126:129], v[6:9]
	v_mfma_f32_16x16x32_f16 v[34:37], v[174:177], v[114:117], v[34:37]
	v_mfma_f32_16x16x32_f16 v[2:5], v[174:177], v[126:129], v[2:5]
	s_cmpk_gt_u32 s61, 0xff
	s_barrier
	s_cbranch_scc1 .LBB10_15
	s_barrier
